# P7 row pass: modulation-constant loads pipelined into spare VGPR quads with counted vmcnt; DOWN expert-GEMM epilogue LDS reads batched; sc1 stores on out-proj epilogue
# speedup vs baseline: 1.0091x; 1.0091x over previous
; __device__ __forceinline__ void phase7(const Args& a, LAS unsigned char* lds, int tid, int lane, int wave) {
;     ...
;             const int r0 = 2 * wave, t0 = base + r0, t1 = t0 + 1;
;             const f32x4* y0p = (const f32x4*)(Y + (size_t)t0 * D) + lane; const f32x4* y1p = (const f32x4*)(Y + (size_t)t1 * D) + lane;
;             const f32x4* x0p = (const f32x4*)(x + (size_t)t0 * D) + lane; const f32x4* x1p = (const f32x4*)(x + (size_t)t1 * D) + lane;
;             f32x4 v0[8], v1[8], xa[8], xb[8]; float ss0 = 0.f, ss1 = 0.f;
; #pragma unroll
;             for (int j = 0; j < 8; ++j) { v0[j] = y0p[64 * j]; v1[j] = y1p[64 * j]; }
; #pragma unroll
;             for (int j = 0; j < 8; ++j) { xa[j] = x0p[64 * j]; xb[j] = x1p[64 * j]; }
; #pragma unroll
;             for (int j = 0; j < 8; ++j) { ss0 += (v0[j].x * v0[j].x + v0[j].y * v0[j].y) + (v0[j].z * v0[j].z + v0[j].w * v0[j].w); ss1 += (v1[j].x * v1[j].x + v1[j].y * v1[j].y) + (v1[j].z * v1[j].z + v1[j].w * v1[j].w); }
;             ss0 = wave_sum(ss0); ss1 = wave_sum(ss1);
;             const float rs0 = 1.0f / sqrtf(ss0 * (1.0f / D) + EPS), rs1 = 1.0f / sqrtf(ss1 * (1.0f / D) + EPS);
.LBB0_1022:
	s_add_i32 s12, s2, s33
	s_ashr_i32 s13, s12, 31
	s_lshl_b64 s[0:1], s[12:13], 13
	v_lshl_add_u64 v[2:3], v[114:115], 0, s[0:1]
	s_or_b32 s14, s12, 1
	global_load_dwordx4 v[50:53], v[2:3], off
	global_load_dwordx4 v[38:41], v[2:3], off offset:1024
	s_ashr_i32 s15, s14, 31
	global_load_dwordx4 v[30:33], v[2:3], off offset:2048
	s_lshl_b64 s[8:9], s[14:15], 13
	v_add_co_u32_e32 v62, vcc, s39, v2
	v_lshl_add_u64 v[4:5], v[114:115], 0, s[8:9]
	s_nop 0
	v_addc_co_u32_e32 v63, vcc, 0, v3, vcc
	global_load_dwordx4 v[54:57], v[4:5], off
	global_load_dwordx4 v[42:45], v[4:5], off offset:1024
	global_load_dwordx4 v[26:29], v[4:5], off offset:2048
	global_load_dwordx4 v[10:13], v[62:63], off
	global_load_dwordx4 v[18:21], v[2:3], off offset:3072
	v_add_co_u32_e32 v64, vcc, s39, v4
	v_lshl_add_u64 v[58:59], v[116:117], 0, s[0:1]
	s_nop 0
	v_addc_co_u32_e32 v65, vcc, 0, v5, vcc
	global_load_dwordx4 v[6:9], v[64:65], off
	global_load_dwordx4 v[14:17], v[4:5], off offset:3072
	v_lshl_add_u64 v[60:61], v[116:117], 0, s[8:9]
	global_load_dwordx4 v[74:77], v[58:59], off
	global_load_dwordx4 v[46:49], v[58:59], off offset:1024
	global_load_dwordx4 v[2:5], v[62:63], off offset:1024
	global_load_dwordx4 v[34:37], v[58:59], off offset:2048
	global_load_dwordx4 v[22:25], v[58:59], off offset:3072
	global_load_dwordx4 v[192:195], v[118:119], off
	global_load_dwordx4 v[82:85], v[62:63], off offset:2048
	global_load_dwordx4 v[66:69], v[62:63], off offset:3072
	global_load_dwordx4 v[86:89], v[64:65], off offset:1024
	global_load_dwordx4 v[196:199], v[60:61], off
	global_load_dwordx4 v[106:109], v[60:61], off offset:1024
	global_load_dwordx4 v[70:73], v[64:65], off offset:2048
	s_nop 0
	global_load_dwordx4 v[62:65], v[64:65], off offset:3072
	v_add_co_u32_e32 v58, vcc, s39, v58
	s_waitcnt vmcnt(22)
	v_mov_b32_e32 v80, v51
	s_waitcnt vmcnt(21)
	v_mov_b32_e32 v81, v39
	v_mov_b32_e32 v92, v53
	v_mov_b32_e32 v93, v41
	v_mov_b32_e32 v78, v50
	v_mov_b32_e32 v79, v38
	v_mov_b32_e32 v90, v52
	v_mov_b32_e32 v91, v40
	s_waitcnt vmcnt(20)
	v_pk_mul_f32 v[94:95], v[32:33], v[32:33]
	v_pk_mul_f32 v[96:97], v[30:31], v[30:31]
	v_pk_mul_f32 v[80:81], v[80:81], v[80:81]
	v_pk_mul_f32 v[92:93], v[92:93], v[92:93]
	v_pk_mov_b32 v[200:201], v[96:97], v[94:95] op_sel:[1,0]
	v_mov_b32_e32 v97, v95
	v_pk_fma_f32 v[78:79], v[78:79], v[78:79], v[80:81]
	v_pk_fma_f32 v[80:81], v[90:91], v[90:91], v[92:93]
	s_waitcnt vmcnt(19)
	v_mov_b32_e32 v100, v55
	s_waitcnt vmcnt(18)
	v_mov_b32_e32 v101, v43
	v_mov_b32_e32 v104, v57
	v_mov_b32_e32 v105, v45
	s_waitcnt vmcnt(17)
	v_pk_mul_f32 v[94:95], v[28:29], v[28:29]
	v_pk_mul_f32 v[202:203], v[26:27], v[26:27]
	s_waitcnt vmcnt(15)
	v_mul_f32_e32 v112, v19, v19
	v_mul_f32_e32 v174, v21, v21
	v_pk_add_f32 v[96:97], v[200:201], v[96:97]
	v_pk_add_f32 v[78:79], v[78:79], v[80:81]
	v_mov_b32_e32 v98, v54
	v_mov_b32_e32 v99, v42
	v_mov_b32_e32 v102, v56
	v_mov_b32_e32 v103, v44
	v_mul_f32_e32 v204, v10, v10
	v_mul_f32_e32 v205, v11, v11
	v_mul_f32_e32 v206, v12, v12
	v_mul_f32_e32 v207, v13, v13
	v_pk_mul_f32 v[90:91], v[100:101], v[100:101]
	v_pk_mul_f32 v[92:93], v[104:105], v[104:105]
	v_pk_mov_b32 v[100:101], v[202:203], v[94:95] op_sel:[1,0]
	v_mov_b32_e32 v203, v95
	v_pk_fma_f32 v[94:95], v[18:19], v[18:19], v[112:113] op_sel_hi:[1,1,0]
	v_pk_fma_f32 v[104:105], v[20:21], v[20:21], v[174:175] op_sel_hi:[1,1,0]
	v_pk_add_f32 v[96:97], v[96:97], v[96:97] op_sel:[0,1] op_sel_hi:[1,0]
	v_pk_add_f32 v[78:79], v[78:79], v[78:79] op_sel:[0,1] op_sel_hi:[1,0]
	v_pk_fma_f32 v[80:81], v[98:99], v[98:99], v[90:91]
	v_pk_fma_f32 v[90:91], v[102:103], v[102:103], v[92:93]
	v_mov_b32_e32 v95, v206
	v_mov_b32_e32 v97, v205
	v_mov_b32_e32 v79, v204
	v_mov_b32_e32 v105, v207
	v_pk_add_f32 v[80:81], v[80:81], v[90:91]
	v_pk_add_f32 v[78:79], v[78:79], v[96:97]
	v_pk_add_f32 v[90:91], v[94:95], v[104:105]
	v_pk_add_f32 v[92:93], v[100:101], v[202:203]
	v_pk_add_f32 v[78:79], v[78:79], v[90:91]
	s_waitcnt vmcnt(14)
	v_mul_f32_e32 v90, v6, v6
	v_pk_add_f32 v[80:81], v[80:81], v[80:81] op_sel:[0,1] op_sel_hi:[1,0]
	v_mul_f32_e32 v94, v7, v7
	v_mov_b32_e32 v81, v90
	v_pk_add_f32 v[90:91], v[92:93], v[92:93] op_sel:[0,1] op_sel_hi:[1,0]
	s_waitcnt vmcnt(13)
	v_mul_f32_e32 v92, v17, v17
	v_mov_b32_e32 v91, v94
	v_pk_add_f32 v[80:81], v[80:81], v[90:91]
	v_mul_f32_e32 v90, v15, v15
	v_mul_f32_e32 v95, v8, v8
	v_mul_f32_e32 v96, v9, v9
	v_pk_fma_f32 v[90:91], v[14:15], v[14:15], v[90:91] op_sel_hi:[1,1,0]
	v_pk_fma_f32 v[92:93], v[16:17], v[16:17], v[92:93] op_sel_hi:[1,1,0]
	v_mov_b32_e32 v91, v95
	v_mov_b32_e32 v93, v96
	v_pk_add_f32 v[90:91], v[90:91], v[92:93]
	s_waitcnt vmcnt(10)
	v_pk_mul_f32 v[92:93], v[2:3], v[2:3]
	v_pk_add_f32 v[80:81], v[80:81], v[90:91]
	v_pk_mul_f32 v[90:91], v[4:5], v[4:5]
	v_pk_add_f32 v[78:79], v[78:79], v[78:79] op_sel:[0,1] op_sel_hi:[1,0]
	v_pk_mov_b32 v[94:95], v[92:93], v[90:91] op_sel:[1,0]
	v_mov_b32_e32 v93, v91
	v_pk_add_f32 v[90:91], v[94:95], v[92:93]
	s_waitcnt vmcnt(4)
	v_pk_mul_f32 v[92:93], v[88:89], v[88:89]
	v_pk_mul_f32 v[94:95], v[86:87], v[86:87]
	v_pk_add_f32 v[90:91], v[90:91], v[90:91] op_sel:[0,1] op_sel_hi:[1,0]
	v_pk_mov_b32 v[96:97], v[94:95], v[92:93] op_sel:[1,0]
	v_mov_b32_e32 v95, v93
	v_pk_add_f32 v[92:93], v[96:97], v[94:95]
	v_mul_f32_e32 v94, v66, v66
	v_mul_f32_e32 v95, v67, v67
	v_mov_b32_e32 v79, v94
	v_mov_b32_e32 v91, v95
	v_pk_add_f32 v[78:79], v[78:79], v[90:91]
	v_mul_f32_e32 v90, v83, v83
	v_mul_f32_e32 v94, v85, v85
	v_mul_f32_e32 v96, v68, v68
	v_mul_f32_e32 v97, v69, v69
	v_pk_fma_f32 v[90:91], v[82:83], v[82:83], v[90:91] op_sel_hi:[1,1,0]
	v_pk_fma_f32 v[94:95], v[84:85], v[84:85], v[94:95] op_sel_hi:[1,1,0]
	v_mov_b32_e32 v91, v96
	v_mov_b32_e32 v95, v97
	v_pk_add_f32 v[90:91], v[90:91], v[94:95]
	s_waitcnt vmcnt(0)
; __device__ __forceinline__ v2u pk4(f32x4 v) { v2u r; r.x = pk2(v.x, v.y); r.y = pk2(v.z, v.w); return r; }
; __device__ __forceinline__ void phase7(const Args& a, LAS unsigned char* lds, int tid, int lane, int wave) {
;     ...
;             ss0 = wave_sum(ss0); ss1 = wave_sum(ss1);
;             const float rs0 = 1.0f / sqrtf(ss0 * (1.0f / D) + EPS), rs1 = 1.0f / sqrtf(ss1 * (1.0f / D) + EPS);
;             float q0 = 0.f, q1 = 0.f;
; #pragma unroll
;             for (int j = 0; j < 8; ++j) { const int k = 4 * lane + 256 * j; const f32x4 A = *(const f32x4*)(ABC + k);
;                 const f32x4 a0 = xa[j] + A * (v0[j] * rs0), a1 = xb[j] + A * (v1[j] * rs1);
;                 *(v2u*)(X1 + (size_t)t0 * D + k) = pk4(a0); *(v2u*)(X1 + (size_t)t1 * D + k) = pk4(a1); v0[j] = a0; v1[j] = a1;
;                 q0 += (a0.x * a0.x + a0.y * a0.y) + (a0.z * a0.z + a0.w * a0.w); q1 += (a1.x * a1.x + a1.y * a1.y) + (a1.z * a1.z + a1.w * a1.w); }
	v_mul_f32_e32 v94, v63, v63
	v_pk_add_f32 v[78:79], v[78:79], v[90:91]
	v_mul_f32_e32 v90, v62, v62
	v_add_f32_e32 v91, v78, v79
	v_pk_add_f32 v[78:79], v[80:81], v[80:81] op_sel:[0,1] op_sel_hi:[1,0]
	v_pk_add_f32 v[80:81], v[92:93], v[92:93] op_sel:[0,1] op_sel_hi:[1,0]
	ds_bpermute_b32 v92, v176, v91
	v_mov_b32_e32 v79, v90
	v_mov_b32_e32 v81, v94
	v_pk_add_f32 v[78:79], v[78:79], v[80:81]
	v_mul_f32_e32 v80, v71, v71
	s_waitcnt lgkmcnt(0)
	v_add_f32_e32 v92, v91, v92
	ds_bpermute_b32 v93, v177, v92
	v_mul_f32_e32 v90, v73, v73
	v_mul_f32_e32 v95, v64, v64
	v_mul_f32_e32 v96, v65, v65
	v_pk_fma_f32 v[80:81], v[70:71], v[70:71], v[80:81] op_sel_hi:[1,1,0]
	v_pk_fma_f32 v[90:91], v[72:73], v[72:73], v[90:91] op_sel_hi:[1,1,0]
	v_mov_b32_e32 v81, v95
	v_mov_b32_e32 v91, v96
	v_pk_add_f32 v[80:81], v[80:81], v[90:91]
	v_addc_co_u32_e32 v59, vcc, 0, v59, vcc
	v_pk_add_f32 v[78:79], v[78:79], v[80:81]
	s_waitcnt lgkmcnt(0)
	v_add_f32_e32 v80, v92, v93
	ds_bpermute_b32 v81, v178, v80
	v_add_f32_e32 v78, v78, v79
	ds_bpermute_b32 v79, v176, v78
	global_load_dwordx4 v[200:203], v[60:61], off offset:2048
	global_load_dwordx4 v[204:207], v[60:61], off offset:3072
	s_waitcnt lgkmcnt(1)
	v_add_f32_e32 v80, v80, v81
	ds_bpermute_b32 v81, v179, v80
	s_waitcnt lgkmcnt(1)
	v_add_f32_e32 v78, v78, v79
	ds_bpermute_b32 v79, v177, v78
	s_waitcnt lgkmcnt(1)
	v_add_f32_e32 v80, v80, v81
	ds_bpermute_b32 v81, v180, v80
	s_waitcnt lgkmcnt(1)
	v_add_f32_e32 v90, v78, v79
	ds_bpermute_b32 v91, v178, v90
	v_add_co_u32_e32 v78, vcc, s39, v60
	s_waitcnt lgkmcnt(1)
	v_add_f32_e32 v60, v80, v81
	v_addc_co_u32_e32 v79, vcc, 0, v61, vcc
	ds_bpermute_b32 v61, v181, v60
	s_waitcnt lgkmcnt(1)
	v_add_f32_e32 v80, v90, v91
	ds_bpermute_b32 v81, v179, v80
	global_load_dwordx4 v[208:211], v[58:59], off
	global_load_dwordx4 v[102:105], v[58:59], off offset:1024
	global_load_dwordx4 v[212:215], v[78:79], off
	global_load_dwordx4 v[98:101], v[78:79], off offset:1024
	s_waitcnt lgkmcnt(1)
	v_add_f32_e32 v60, v60, v61
	v_fmamk_f32 v60, v60, 0x3a000000, v186
	s_waitcnt lgkmcnt(0)
	v_add_f32_e32 v80, v80, v81
	v_mul_f32_e32 v61, 0x4f800000, v60
	v_cmp_gt_f32_e32 vcc, s40, v60
	ds_bpermute_b32 v81, v180, v80
	s_waitcnt lgkmcnt(0)
	v_add_f32_e32 v112, v80, v81
	v_cndmask_b32_e32 v94, v60, v61, vcc
	v_sqrt_f32_e32 v95, v94
	ds_bpermute_b32 v174, v181, v112
	global_load_dwordx4 v[90:93], v[58:59], off offset:2048
	s_nop 0
	global_load_dwordx4 v[58:61], v[58:59], off offset:3072
	v_add_u32_e32 v80, -1, v95
	v_fma_f32 v81, -v80, v95, v94
	v_cmp_ge_f32_e64 s[8:9], 0, v81
	v_add_u32_e32 v81, 1, v95
	s_waitcnt lgkmcnt(0)
	v_add_f32_e32 v112, v112, v174
	v_cndmask_b32_e64 v80, v95, v80, s[8:9]
	v_fma_f32 v95, -v81, v95, v94
	v_cmp_lt_f32_e64 s[8:9], 0, v95
	v_fmamk_f32 v112, v112, 0x3a000000, v186
	v_mul_f32_e32 v220, 0x4f800000, v112
	v_cndmask_b32_e64 v80, v80, v81, s[8:9]
	v_mul_f32_e32 v81, 0x37800000, v80
	v_cndmask_b32_e32 v80, v80, v81, vcc
	v_cmp_class_f32_e32 vcc, v94, v187
	v_cmp_gt_f32_e64 s[8:9], s40, v112
	s_nop 0
	v_cndmask_b32_e32 v216, v80, v94, vcc
	v_div_scale_f32 v217, s[0:1], v216, v216, 1.0
	v_rcp_f32_e32 v218, v217
	v_cndmask_b32_e64 v112, v112, v220, s[8:9]
	v_sqrt_f32_e32 v220, v112
	global_load_dwordx4 v[94:97], v[78:79], off offset:2048
	s_nop 0
	global_load_dwordx4 v[78:81], v[78:79], off offset:3072
	global_load_dwordx4 v[222:225], v[120:121], off
	global_load_dwordx4 v[226:229], v[122:123], off
	global_load_dwordx4 v[230:233], v[124:125], off
	global_load_dwordx4 v[234:237], v[126:127], off
	v_fma_f32 v174, -v217, v218, 1.0
	v_fmac_f32_e32 v218, v174, v218
	v_div_scale_f32 v174, vcc, 1.0, v216, 1.0
	v_mul_f32_e32 v219, v174, v218
	v_fma_f32 v221, -v217, v219, v174
	v_fmac_f32_e32 v219, v221, v218
	v_fma_f32 v174, -v217, v219, v174
	v_add_u32_e32 v217, -1, v220
	v_fma_f32 v221, -v217, v220, v112
	v_cmp_ge_f32_e64 s[10:11], 0, v221
	v_add_u32_e32 v221, 1, v220
	v_div_fmas_f32 v174, v174, v218, v219
	v_cndmask_b32_e64 v217, v220, v217, s[10:11]
	v_fma_f32 v220, -v221, v220, v112
	v_cmp_lt_f32_e64 s[10:11], 0, v220
	v_div_fixup_f32 v174, v174, v216, 1.0
	v_pk_mul_f32 v[38:39], v[38:39], v[174:175] op_sel_hi:[1,0]
	v_cndmask_b32_e64 v217, v217, v221, s[10:11]
	v_mul_f32_e32 v220, 0x37800000, v217
	v_cndmask_b32_e64 v217, v217, v220, s[8:9]
	v_cmp_class_f32_e64 s[8:9], v112, v187
	s_lshl_b64 s[10:11], s[14:15], 12
	v_pk_mul_f32 v[40:41], v[40:41], v[174:175] op_sel_hi:[1,0]
	v_cndmask_b32_e64 v112, v217, v112, s[8:9]
	v_div_scale_f32 v217, s[0:1], v112, v112, 1.0
	v_rcp_f32_e32 v220, v217
	s_lshl_b64 s[8:9], s[12:13], 12
	v_pk_mul_f32 v[18:19], v[18:19], v[174:175] op_sel_hi:[1,0]
	v_pk_mul_f32 v[20:21], v[20:21], v[174:175] op_sel_hi:[1,0]
	v_fma_f32 v216, -v217, v220, 1.0
	v_fmac_f32_e32 v220, v216, v220
	v_div_scale_f32 v216, vcc, 1.0, v112, 1.0
	v_mul_f32_e32 v218, v216, v220
	v_fma_f32 v219, -v217, v218, v216
	v_fmac_f32_e32 v218, v219, v220
	v_fma_f32 v216, -v217, v218, v216
	v_div_fmas_f32 v216, v216, v220, v218
	v_div_fixup_f32 v112, v216, v112, 1.0
	v_pk_mul_f32 v[216:217], v[50:51], v[174:175] op_sel_hi:[1,0]
	v_pk_mul_f32 v[50:51], v[52:53], v[174:175] op_sel_hi:[1,0]
	v_pk_fma_f32 v[52:53], v[192:193], v[216:217], v[74:75]
	v_pk_fma_f32 v[50:51], v[194:195], v[50:51], v[76:77]
	v_pk_mul_f32 v[74:75], v[54:55], v[112:113] op_sel_hi:[1,0]
	v_pk_mul_f32 v[54:55], v[56:57], v[112:113] op_sel_hi:[1,0]
	v_pk_fma_f32 v[56:57], v[192:193], v[74:75], v[196:197]
	v_pk_fma_f32 v[54:55], v[194:195], v[54:55], v[198:199]
	v_cvt_pk_bf16_f32 v76, v52, v53
	v_cvt_pk_bf16_f32 v77, v50, v51
	v_lshl_add_u64 v[74:75], v[166:167], 0, s[8:9]
	global_store_dwordx2 v[74:75], v[76:77], off
	v_cvt_pk_bf16_f32 v192, v56, v57
	v_cvt_pk_bf16_f32 v193, v54, v55
	v_lshl_add_u64 v[76:77], v[166:167], 0, s[10:11]
	global_store_dwordx2 v[76:77], v[192:193], off
	v_pk_mul_f32 v[14:15], v[14:15], v[112:113] op_sel_hi:[1,0]
	v_pk_mul_f32 v[16:17], v[16:17], v[112:113] op_sel_hi:[1,0]
	v_pk_mul_f32 v[10:11], v[10:11], v[174:175] op_sel_hi:[1,0]
	v_pk_mul_f32 v[12:13], v[12:13], v[174:175] op_sel_hi:[1,0]
	v_pk_mul_f32 v[6:7], v[6:7], v[112:113] op_sel_hi:[1,0]
	v_pk_mul_f32 v[8:9], v[8:9], v[112:113] op_sel_hi:[1,0]
	v_pk_mul_f32 v[2:3], v[2:3], v[174:175] op_sel_hi:[1,0]
	v_pk_mul_f32 v[4:5], v[4:5], v[174:175] op_sel_hi:[1,0]
	v_pk_mul_f32 v[70:71], v[70:71], v[112:113] op_sel_hi:[1,0]
	v_pk_mul_f32 v[72:73], v[72:73], v[112:113] op_sel_hi:[1,0]
	s_add_i32 s12, s61, 0x4000
	s_add_i32 s13, s61, 0x4400
	s_add_i32 s14, s61, 0x4800
	s_add_i32 s15, s61, 0x4c00
	s_waitcnt vmcnt(5)
; __device__ __forceinline__ v2u pk4(f32x4 v) { v2u r; r.x = pk2(v.x, v.y); r.y = pk2(v.z, v.w); return r; }
; __device__ __forceinline__ void phase7(const Args& a, LAS unsigned char* lds, int tid, int lane, int wave) {
;     ...
;             for (int j = 0; j < 8; ++j) { const int k = 4 * lane + 256 * j; const f32x4 A = *(const f32x4*)(ABC + k);
;                 const f32x4 a0 = xa[j] + A * (v0[j] * rs0), a1 = xb[j] + A * (v1[j] * rs1);
;                 *(v2u*)(X1 + (size_t)t0 * D + k) = pk4(a0); *(v2u*)(X1 + (size_t)t1 * D + k) = pk4(a1); v0[j] = a0; v1[j] = a1;
;                 q0 += (a0.x * a0.x + a0.y * a0.y) + (a0.z * a0.z + a0.w * a0.w); q1 += (a1.x * a1.x + a1.y * a1.y) + (a1.z * a1.z + a1.w * a1.w); }
	v_pk_fma_f32 v[48:49], v[40:41], v[224:225], v[48:49]
	v_pk_fma_f32 v[46:47], v[38:39], v[222:223], v[46:47]
	v_pk_mul_f32 v[40:41], v[42:43], v[112:113] op_sel_hi:[1, 0]
	v_pk_mul_f32 v[38:39], v[44:45], v[112:113] op_sel_hi:[1, 0]
	v_pk_fma_f32 v[40:41], v[222:223], v[40:41], v[106:107]
	v_pk_fma_f32 v[38:39], v[224:225], v[38:39], v[108:109]
	global_load_dwordx4 v[222:225], v[128:129], off
	v_cvt_pk_bf16_f32 v42, v46, v47
	v_cvt_pk_bf16_f32 v43, v48, v49
	global_store_dwordx2 v[74:75], v[42:43], off offset:512
	v_cvt_pk_bf16_f32 v42, v40, v41
	v_cvt_pk_bf16_f32 v43, v38, v39
	global_store_dwordx2 v[76:77], v[42:43], off offset:512
	v_pk_mul_f32 v[106:107], v[30:31], v[174:175] op_sel_hi:[1, 0]
	v_pk_mul_f32 v[30:31], v[32:33], v[174:175] op_sel_hi:[1, 0]
	v_pk_mul_f32 v[108:109], v[26:27], v[112:113] op_sel_hi:[1, 0]
	v_pk_mul_f32 v[26:27], v[28:29], v[112:113] op_sel_hi:[1, 0]
	v_mov_b32_e32 v194, v55
	v_mov_b32_e32 v195, v39
	v_mov_b32_e32 v192, v54
	v_mov_b32_e32 v193, v38
	s_waitcnt vmcnt(7)
	v_pk_fma_f32 v[30:31], v[30:31], v[228:229], v[36:37]
	v_pk_fma_f32 v[32:33], v[106:107], v[226:227], v[34:35]
	v_pk_fma_f32 v[26:27], v[228:229], v[26:27], v[202:203]
	v_pk_fma_f32 v[28:29], v[226:227], v[108:109], v[200:201]
	global_load_dwordx4 v[226:229], v[130:131], off
	v_cvt_pk_bf16_f32 v34, v32, v33
	v_cvt_pk_bf16_f32 v35, v30, v31
	v_cvt_pk_bf16_f32 v36, v28, v29
	v_cvt_pk_bf16_f32 v37, v26, v27
	global_store_dwordx2 v[74:75], v[34:35], off offset:1024
	global_store_dwordx2 v[76:77], v[36:37], off offset:1024
	v_mov_b32_e32 v108, v57
	v_mov_b32_e32 v109, v41
	v_mov_b32_e32 v106, v56
	v_mov_b32_e32 v107, v40
	s_waitcnt vmcnt(9)
	v_pk_fma_f32 v[24:25], v[20:21], v[232:233], v[24:25]
	v_pk_fma_f32 v[22:23], v[18:19], v[230:231], v[22:23]
	v_pk_fma_f32 v[18:19], v[16:17], v[232:233], v[206:207]
	v_pk_fma_f32 v[20:21], v[14:15], v[230:231], v[204:205]
	global_load_dwordx4 v[230:233], v[132:133], off
	v_cvt_pk_bf16_f32 v14, v22, v23
	v_cvt_pk_bf16_f32 v15, v24, v25
	v_cvt_pk_bf16_f32 v16, v20, v21
	v_cvt_pk_bf16_f32 v17, v18, v19
	global_store_dwordx2 v[74:75], v[14:15], off offset:1536
	global_store_dwordx2 v[76:77], v[16:17], off offset:1536
	s_waitcnt vmcnt(11)
	v_pk_fma_f32 v[14:15], v[12:13], v[236:237], v[210:211]
	v_pk_fma_f32 v[16:17], v[10:11], v[234:235], v[208:209]
	v_pk_fma_f32 v[10:11], v[8:9], v[236:237], v[214:215]
	v_pk_fma_f32 v[12:13], v[6:7], v[234:235], v[212:213]
	v_cvt_pk_bf16_f32 v6, v16, v17
	v_cvt_pk_bf16_f32 v7, v14, v15
	v_cvt_pk_bf16_f32 v8, v12, v13
	v_cvt_pk_bf16_f32 v9, v10, v11
	global_store_dwordx2 v[74:75], v[6:7], off offset:2048
	global_store_dwordx2 v[76:77], v[8:9], off offset:2048
	v_pk_mul_f32 v[36:37], v[86:87], v[112:113] op_sel_hi:[1, 0]
	v_pk_mul_f32 v[34:35], v[88:89], v[112:113] op_sel_hi:[1, 0]
	v_pk_mul_f32 v[86:87], v[62:63], v[112:113] op_sel_hi:[1, 0]
	v_pk_mul_f32 v[88:89], v[64:65], v[112:113] op_sel_hi:[1, 0]
	s_waitcnt vmcnt(10)
	v_pk_fma_f32 v[42:43], v[4:5], v[224:225], v[104:105]
	v_pk_fma_f32 v[44:45], v[2:3], v[222:223], v[102:103]
	v_pk_fma_f32 v[34:35], v[34:35], v[224:225], v[100:101]
	v_pk_fma_f32 v[36:37], v[36:37], v[222:223], v[98:99]
	v_cvt_pk_bf16_f32 v2, v44, v45
	v_cvt_pk_bf16_f32 v3, v42, v43
	v_cvt_pk_bf16_f32 v4, v36, v37
	v_cvt_pk_bf16_f32 v5, v34, v35
	global_store_dwordx2 v[74:75], v[2:3], off offset:2560
	global_store_dwordx2 v[76:77], v[4:5], off offset:2560
	v_pk_mul_f32 v[6:7], v[82:83], v[174:175] op_sel_hi:[1, 0]
	v_pk_mul_f32 v[8:9], v[84:85], v[174:175] op_sel_hi:[1, 0]
	v_pk_mul_f32 v[82:83], v[66:67], v[174:175] op_sel_hi:[1,0]
	v_pk_mul_f32 v[84:85], v[68:69], v[174:175] op_sel_hi:[1,0]
	v_mov_b32_e32 v100, v53
	v_mov_b32_e32 v104, v51
	v_mov_b32_e32 v101, v47
	v_mov_b32_e32 v105, v49
	v_mov_b32_e32 v98, v52
	v_mov_b32_e32 v102, v50
	v_mov_b32_e32 v99, v46
	v_mov_b32_e32 v103, v48
	s_waitcnt vmcnt(9)
	v_pk_fma_f32 v[66:67], v[8:9], v[228:229], v[92:93]
	v_pk_fma_f32 v[68:69], v[6:7], v[226:227], v[90:91]
	v_pk_fma_f32 v[62:63], v[72:73], v[228:229], v[96:97]
	v_pk_fma_f32 v[64:65], v[70:71], v[226:227], v[94:95]
	v_cvt_pk_bf16_f32 v2, v68, v69
	v_cvt_pk_bf16_f32 v3, v66, v67
	v_cvt_pk_bf16_f32 v4, v64, v65
	v_cvt_pk_bf16_f32 v5, v62, v63
	global_store_dwordx2 v[74:75], v[2:3], off offset:3072
	global_store_dwordx2 v[76:77], v[4:5], off offset:3072
	v_pk_mul_f32 v[6:7], v[100:101], v[100:101]
	v_pk_mul_f32 v[8:9], v[104:105], v[104:105]
	v_pk_mul_f32 v[70:71], v[108:109], v[108:109]
	v_pk_mul_f32 v[72:73], v[194:195], v[194:195]
	v_pk_fma_f32 v[6:7], v[98:99], v[98:99], v[6:7]
	v_pk_fma_f32 v[8:9], v[102:103], v[102:103], v[8:9]
	v_pk_fma_f32 v[70:71], v[106:107], v[106:107], v[70:71]
	v_pk_fma_f32 v[72:73], v[192:193], v[192:193], v[72:73]
	v_pk_add_f32 v[6:7], v[6:7], v[8:9]
	v_pk_add_f32 v[8:9], v[70:71], v[72:73]
	v_pk_mul_f32 v[70:71], v[32:33], v[32:33]
	v_pk_mul_f32 v[72:73], v[30:31], v[30:31]
	v_pk_mul_f32 v[90:91], v[28:29], v[28:29]
	v_pk_mul_f32 v[92:93], v[26:27], v[26:27]
	v_pk_mov_b32 v[94:95], v[70:71], v[72:73] op_sel:[1,0]
	v_mov_b32_e32 v71, v73
	v_pk_mov_b32 v[72:73], v[90:91], v[92:93] op_sel:[1,0]
	v_mov_b32_e32 v91, v93
	v_pk_add_f32 v[70:71], v[94:95], v[70:71]
	v_pk_add_f32 v[72:73], v[72:73], v[90:91]
	v_mul_f32_e32 v90, v23, v23
	v_mul_f32_e32 v92, v25, v25
	v_mul_f32_e32 v94, v21, v21
	v_mul_f32_e32 v96, v19, v19
	v_pk_add_f32 v[6:7], v[6:7], v[6:7] op_sel:[0,1] op_sel_hi:[1,0]
	v_pk_add_f32 v[8:9], v[8:9], v[8:9] op_sel:[0,1] op_sel_hi:[1,0]
	v_pk_add_f32 v[70:71], v[70:71], v[70:71] op_sel:[0,1] op_sel_hi:[1,0]
	v_pk_add_f32 v[72:73], v[72:73], v[72:73] op_sel:[0,1] op_sel_hi:[1,0]
	v_pk_fma_f32 v[90:91], v[22:23], v[22:23], v[90:91] op_sel_hi:[1,1,0]
; __device__ __forceinline__ void phase7(const Args& a, LAS unsigned char* lds, int tid, int lane, int wave) {
;     ...
;                 q0 += (a0.x * a0.x + a0.y * a0.y) + (a0.z * a0.z + a0.w * a0.w); q1 += (a1.x * a1.x + a1.y * a1.y) + (a1.z * a1.z + a1.w * a1.w); }
;             q0 = wave_sum(q0); q1 = wave_sum(q1);
;             const float rt0 = 1.0f / sqrtf(q0 * (1.0f / D) + EPS), rt1 = 1.0f / sqrtf(q1 * (1.0f / D) + EPS);
; #pragma unroll
;             for (int j = 0; j < 8; ++j) { const int k = 4 * lane + 256 * j; const f32x4 B = *(const f32x4*)(ABC + 2048 + k), C = *(const f32x4*)(ABC + 4096 + k);
	v_pk_fma_f32 v[92:93], v[24:25], v[24:25], v[92:93] op_sel_hi:[1,1,0]
	v_pk_fma_f32 v[94:95], v[20:21], v[20:21], v[94:95] op_sel_hi:[1,1,0]
	v_pk_fma_f32 v[96:97], v[18:19], v[18:19], v[96:97] op_sel_hi:[1,1,0]
	v_mul_f32_e32 v98, v10, v10
	v_mul_f32_e32 v99, v11, v11
	v_mul_f32_e32 v7, v16, v16
	v_mul_f32_e32 v71, v17, v17
	v_mul_f32_e32 v91, v14, v14
	v_mul_f32_e32 v93, v15, v15
	v_mul_f32_e32 v95, v12, v12
	v_mul_f32_e32 v97, v13, v13
	v_mov_b32_e32 v73, v98
	v_mov_b32_e32 v9, v99
	v_pk_add_f32 v[6:7], v[6:7], v[70:71]
	v_pk_add_f32 v[70:71], v[90:91], v[92:93]
	v_pk_add_f32 v[90:91], v[94:95], v[96:97]
	v_pk_add_f32 v[8:9], v[72:73], v[8:9]
	v_pk_add_f32 v[6:7], v[6:7], v[70:71]
	v_pk_add_f32 v[8:9], v[90:91], v[8:9]
	v_pk_mul_f32 v[70:71], v[44:45], v[44:45]
	v_pk_mul_f32 v[72:73], v[42:43], v[42:43]
	v_pk_mul_f32 v[90:91], v[36:37], v[36:37]
	v_pk_mul_f32 v[92:93], v[34:35], v[34:35]
	v_pk_mov_b32 v[94:95], v[70:71], v[72:73] op_sel:[1,0]
	v_mov_b32_e32 v71, v73
	v_pk_mov_b32 v[72:73], v[90:91], v[92:93] op_sel:[1,0]
	v_mov_b32_e32 v91, v93
	v_pk_add_f32 v[70:71], v[94:95], v[70:71]
	v_pk_add_f32 v[72:73], v[72:73], v[90:91]
	v_pk_add_f32 v[90:91], v[70:71], v[70:71] op_sel:[0,1] op_sel_hi:[1,0]
	v_pk_add_f32 v[92:93], v[72:73], v[72:73] op_sel:[0,1] op_sel_hi:[1,0]
	v_mul_f32_e32 v70, v69, v69
	v_mul_f32_e32 v72, v67, v67
	v_mul_f32_e32 v94, v65, v65
	v_mul_f32_e32 v96, v63, v63
	v_pk_add_f32 v[6:7], v[6:7], v[6:7] op_sel:[0,1] op_sel_hi:[1,0]
	v_pk_add_f32 v[8:9], v[8:9], v[8:9] op_sel:[0,1] op_sel_hi:[1,0]
	v_pk_fma_f32 v[98:99], v[68:69], v[68:69], v[70:71] op_sel_hi:[1,1,0]
	v_pk_fma_f32 v[100:101], v[66:67], v[66:67], v[72:73] op_sel_hi:[1,1,0]
	v_pk_fma_f32 v[94:95], v[64:65], v[64:65], v[94:95] op_sel_hi:[1,1,0]
	v_pk_fma_f32 v[96:97], v[62:63], v[62:63], v[96:97] op_sel_hi:[1,1,0]
	s_waitcnt vmcnt(8)
	v_pk_fma_f32 v[70:71], v[84:85], v[232:233], v[60:61]
	v_pk_fma_f32 v[72:73], v[82:83], v[230:231], v[58:59]
	v_pk_fma_f32 v[58:59], v[88:89], v[232:233], v[80:81]
	v_pk_fma_f32 v[60:61], v[86:87], v[230:231], v[78:79]
	v_mul_f32_e32 v7, v72, v72
	v_mul_f32_e32 v91, v73, v73
	v_mul_f32_e32 v99, v70, v70
	v_mul_f32_e32 v101, v71, v71
	v_mul_f32_e32 v9, v60, v60
	v_mul_f32_e32 v93, v61, v61
	v_mul_f32_e32 v95, v58, v58
	v_mul_f32_e32 v97, v59, v59
	v_pk_add_f32 v[2:3], v[6:7], v[90:91]
	v_pk_add_f32 v[4:5], v[98:99], v[100:101]
	v_pk_add_f32 v[6:7], v[8:9], v[92:93]
	v_pk_add_f32 v[8:9], v[94:95], v[96:97]
	v_pk_add_f32 v[2:3], v[2:3], v[4:5]
	v_pk_add_f32 v[4:5], v[6:7], v[8:9]
	v_add_f32_e32 v2, v2, v3
	v_add_f32_e32 v3, v4, v5
	ds_bpermute_b32 v4, v176, v2
	ds_bpermute_b32 v5, v176, v3
	s_waitcnt lgkmcnt(1)
	v_add_f32_e32 v4, v2, v4
	s_waitcnt lgkmcnt(0)
	v_add_f32_e32 v5, v3, v5
	ds_bpermute_b32 v6, v177, v4
	ds_bpermute_b32 v7, v177, v5
	v_cvt_pk_bf16_f32 v2, v72, v73
	v_cvt_pk_bf16_f32 v3, v70, v71
	global_store_dwordx2 v[74:75], v[2:3], off offset:3584
	s_waitcnt lgkmcnt(1)
	v_add_f32_e32 v6, v4, v6
	s_waitcnt lgkmcnt(0)
	v_add_f32_e32 v7, v5, v7
	ds_bpermute_b32 v8, v178, v6
	ds_bpermute_b32 v9, v178, v7
	v_cvt_pk_bf16_f32 v4, v60, v61
	v_cvt_pk_bf16_f32 v5, v58, v59
	global_store_dwordx2 v[76:77], v[4:5], off offset:3584
	s_waitcnt lgkmcnt(1)
	v_add_f32_e32 v2, v6, v8
	s_waitcnt lgkmcnt(0)
	v_add_f32_e32 v3, v7, v9
	global_load_dwordx4 v[6:9], v[134:135], off
	global_load_dwordx4 v[80:83], v[136:137], off
	ds_bpermute_b32 v74, v179, v2
	ds_bpermute_b32 v75, v179, v3
	v_lshl_add_u64 v[76:77], v[168:169], 0, s[10:11]
	s_waitcnt lgkmcnt(1)
	v_add_f32_e32 v2, v2, v74
	s_waitcnt lgkmcnt(0)
	v_add_f32_e32 v3, v3, v75
	ds_bpermute_b32 v4, v180, v2
	ds_bpermute_b32 v5, v180, v3
	v_lshl_add_u64 v[74:75], v[168:169], 0, s[8:9]
	s_waitcnt lgkmcnt(1)
	v_add_f32_e32 v2, v2, v4
	s_waitcnt lgkmcnt(0)
	v_add_f32_e32 v3, v3, v5
	ds_bpermute_b32 v4, v181, v2
	ds_bpermute_b32 v5, v181, v3
	s_waitcnt lgkmcnt(1)
	v_add_f32_e32 v2, v2, v4
	s_waitcnt lgkmcnt(0)
	v_add_f32_e32 v3, v3, v5
	v_fmamk_f32 v2, v2, 0x3a000000, v186
	v_fmamk_f32 v3, v3, 0x3a000000, v186
	v_mul_f32_e32 v4, 0x4f800000, v2
	v_cmp_gt_f32_e32 vcc, s40, v2
	v_mul_f32_e32 v5, 0x4f800000, v3
	v_cmp_gt_f32_e64 s[8:9], s40, v3
	v_cndmask_b32_e32 v2, v2, v4, vcc
	v_sqrt_f32_e32 v4, v2
	v_cndmask_b32_e64 v3, v3, v5, s[8:9]
	v_sqrt_f32_e32 v5, v3
	v_add_u32_e32 v78, -1, v4
	v_fma_f32 v86, -v78, v4, v2
	v_add_u32_e32 v84, -1, v5
	v_add_u32_e32 v79, 1, v4
	v_fma_f32 v88, -v84, v5, v3
	v_cmp_ge_f32_e64 s[10:11], 0, v86
	v_add_u32_e32 v85, 1, v5
	v_fma_f32 v87, -v79, v4, v2
	v_cndmask_b32_e64 v4, v4, v78, s[10:11]
	v_cmp_ge_f32_e64 s[10:11], 0, v88
	v_fma_f32 v89, -v85, v5, v3
	s_nop 0
	v_cndmask_b32_e64 v5, v5, v84, s[10:11]
	v_cmp_lt_f32_e64 s[10:11], 0, v87
	s_nop 1
	v_cndmask_b32_e64 v4, v4, v79, s[10:11]
	v_cmp_lt_f32_e64 s[10:11], 0, v89
	v_mul_f32_e32 v78, 0x37800000, v4
	v_cndmask_b32_e32 v4, v4, v78, vcc
	v_cndmask_b32_e64 v5, v5, v85, s[10:11]
	v_mul_f32_e32 v79, 0x37800000, v5
	v_cmp_class_f32_e32 vcc, v2, v187
	v_cndmask_b32_e64 v5, v5, v79, s[8:9]
	s_or_b32 s10, s61, 0x3800
	v_cndmask_b32_e32 v2, v4, v2, vcc
	v_cmp_class_f32_e32 vcc, v3, v187
	v_div_scale_f32 v4, s[0:1], v2, v2, 1.0
	s_nop 0
	v_cndmask_b32_e32 v3, v5, v3, vcc
	v_div_scale_f32 v78, s[0:1], v3, v3, 1.0
	v_rcp_f32_e32 v79, v4
	v_rcp_f32_e32 v85, v78
	v_div_scale_f32 v5, vcc, 1.0, v2, 1.0
	v_fma_f32 v86, -v4, v79, 1.0
	v_fma_f32 v87, -v78, v85, 1.0
	v_fmac_f32_e32 v79, v86, v79
	v_div_scale_f32 v84, s[8:9], 1.0, v3, 1.0
	v_fmac_f32_e32 v85, v87, v85
	v_mul_f32_e32 v86, v5, v79
	v_mul_f32_e32 v87, v84, v85
	v_fma_f32 v88, -v4, v86, v5
	v_fma_f32 v89, -v78, v87, v84
	v_fmac_f32_e32 v86, v88, v79
	v_fmac_f32_e32 v87, v89, v85
	v_fma_f32 v4, -v4, v86, v5
	v_fma_f32 v5, -v78, v87, v84
	v_div_fmas_f32 v4, v4, v79, v86
	s_mov_b64 vcc, s[8:9]
	v_div_fixup_f32 v84, v4, v2, 1.0
	v_div_fmas_f32 v2, v5, v85, v87
	v_div_fixup_f32 v78, v2, v3, 1.0
	v_pk_mul_f32 v[2:3], v[52:53], v[84:85] op_sel_hi:[1,0]
	v_pk_mul_f32 v[4:5], v[50:51], v[84:85] op_sel_hi:[1,0]
	v_pk_mul_f32 v[50:51], v[56:57], v[78:79] op_sel_hi:[1,0]
	v_pk_mul_f32 v[52:53], v[54:55], v[78:79] op_sel_hi:[1,0]
	global_load_dwordx4 v[222:225], v[138:139], off
	global_load_dwordx4 v[226:229], v[140:141], off
	global_load_dwordx4 v[230:233], v[142:143], off
	global_load_dwordx4 v[234:237], v[144:145], off
	s_waitcnt vmcnt(4)
; #define LAS __attribute__((address_space(3)))
; __device__ __forceinline__ v2u pk4(f32x4 v) { v2u r; r.x = pk2(v.x, v.y); r.y = pk2(v.z, v.w); return r; }
; __device__ __forceinline__ void phase7(const Args& a, LAS unsigned char* lds, int tid, int lane, int wave) {
;     ...
; #pragma unroll
;             for (int j = 0; j < 8; ++j) { const int k = 4 * lane + 256 * j; const f32x4 B = *(const f32x4*)(ABC + 2048 + k), C = *(const f32x4*)(ABC + 4096 + k);
;                 const f32x4 h0 = (v0[j] * rt0) * B + C, h1 = (v1[j] * rt1) * B + C;
;                 *(v2u*)(HN + (size_t)t0 * D + k) = pk4(h0); *(v2u*)(HN + (size_t)t1 * D + k) = pk4(h1);
;                 *(LAS f32x4*)(H2 + r0 * HP + k) = h0; *(LAS f32x4*)(H2 + (r0 + 1) * HP + k) = h1; }
	v_pk_fma_f32 v[4:5], v[8:9], v[4:5], v[82:83]
	v_pk_fma_f32 v[2:3], v[6:7], v[2:3], v[80:81]
	v_pk_fma_f32 v[8:9], v[8:9], v[52:53], v[82:83]
	v_pk_fma_f32 v[6:7], v[6:7], v[50:51], v[80:81]
	global_load_dwordx4 v[50:53], v[146:147], off
	global_load_dwordx4 v[54:57], v[148:149], off
	v_cvt_pk_bf16_f32 v238, v2, v3
	v_cvt_pk_bf16_f32 v239, v4, v5
	v_cvt_pk_bf16_f32 v240, v6, v7
	v_cvt_pk_bf16_f32 v241, v8, v9
	global_store_dwordx2 v[74:75], v[238:239], off
	global_store_dwordx2 v[76:77], v[240:241], off
	v_pk_mul_f32 v[48:49], v[48:49], v[84:85] op_sel_hi:[1,0]
	v_pk_mul_f32 v[46:47], v[46:47], v[84:85] op_sel_hi:[1,0]
	v_pk_mul_f32 v[80:81], v[38:39], v[78:79] op_sel_hi:[1,0]
	v_pk_mul_f32 v[82:83], v[40:41], v[78:79] op_sel_hi:[1,0]
	v_pk_mul_f32 v[30:31], v[30:31], v[84:85] op_sel_hi:[1,0]
	v_pk_mul_f32 v[32:33], v[32:33], v[84:85] op_sel_hi:[1,0]
	v_pk_mul_f32 v[24:25], v[24:25], v[84:85] op_sel_hi:[1,0]
	v_pk_mul_f32 v[22:23], v[22:23], v[84:85] op_sel_hi:[1,0]
	v_pk_mul_f32 v[14:15], v[14:15], v[84:85] op_sel_hi:[1,0]
	v_pk_mul_f32 v[16:17], v[16:17], v[84:85] op_sel_hi:[1,0]
	v_pk_mul_f32 v[42:43], v[42:43], v[84:85] op_sel_hi:[1,0]
	v_pk_mul_f32 v[44:45], v[44:45], v[84:85] op_sel_hi:[1,0]
	v_pk_mul_f32 v[66:67], v[66:67], v[84:85] op_sel_hi:[1,0]
	v_pk_mul_f32 v[68:69], v[68:69], v[84:85] op_sel_hi:[1,0]
	v_pk_mul_f32 v[70:71], v[70:71], v[84:85] op_sel_hi:[1,0]
	v_pk_mul_f32 v[72:73], v[72:73], v[84:85] op_sel_hi:[1,0]
	v_pk_mul_f32 v[58:59], v[58:59], v[78:79] op_sel_hi:[1,0]
	v_pk_mul_f32 v[60:61], v[60:61], v[78:79] op_sel_hi:[1,0]
	s_or_b32 s0, s61, 0x800
	s_or_b32 s1, s61, 0x2c00
	s_or_b32 s8, s61, 0x3000
	s_or_b32 s9, s61, 0x3400
	s_or_b32 s11, s61, 0x3c00
	s_waitcnt vmcnt(6)
	v_pk_fma_f32 v[38:39], v[46:47], v[222:223], v[226:227]
	v_pk_fma_f32 v[40:41], v[48:49], v[224:225], v[228:229]
	v_pk_fma_f32 v[46:47], v[222:223], v[82:83], v[226:227]
	v_pk_fma_f32 v[48:49], v[224:225], v[80:81], v[228:229]
	global_load_dwordx4 v[222:225], v[150:151], off
	global_load_dwordx4 v[226:229], v[152:153], off
	v_cvt_pk_bf16_f32 v238, v38, v39
	v_cvt_pk_bf16_f32 v239, v40, v41
	v_cvt_pk_bf16_f32 v240, v46, v47
	v_cvt_pk_bf16_f32 v241, v48, v49
	global_store_dwordx2 v[74:75], v[238:239], off offset:512
	global_store_dwordx2 v[76:77], v[240:241], off offset:512
	v_pk_mul_f32 v[80:81], v[26:27], v[78:79] op_sel_hi:[1,0]
	v_pk_mul_f32 v[82:83], v[28:29], v[78:79] op_sel_hi:[1,0]
	s_waitcnt vmcnt(8)
	v_pk_fma_f32 v[26:27], v[32:33], v[230:231], v[234:235]
	v_pk_fma_f32 v[28:29], v[30:31], v[232:233], v[236:237]
	v_pk_fma_f32 v[30:31], v[82:83], v[230:231], v[234:235]
	v_pk_fma_f32 v[32:33], v[80:81], v[232:233], v[236:237]
	global_load_dwordx4 v[230:233], v[154:155], off
	global_load_dwordx4 v[234:237], v[156:157], off
	v_cvt_pk_bf16_f32 v238, v26, v27
	v_cvt_pk_bf16_f32 v239, v28, v29
	v_cvt_pk_bf16_f32 v240, v30, v31
	v_cvt_pk_bf16_f32 v241, v32, v33
	global_store_dwordx2 v[74:75], v[238:239], off offset:1024
	global_store_dwordx2 v[76:77], v[240:241], off offset:1024
	v_pk_mul_f32 v[80:81], v[18:19], v[78:79] op_sel_hi:[1,0]
	v_pk_mul_f32 v[82:83], v[20:21], v[78:79] op_sel_hi:[1,0]
	s_waitcnt vmcnt(10)
	v_pk_fma_f32 v[18:19], v[22:23], v[50:51], v[54:55]
	v_pk_fma_f32 v[20:21], v[24:25], v[52:53], v[56:57]
	v_pk_fma_f32 v[22:23], v[82:83], v[50:51], v[54:55]
	v_pk_fma_f32 v[24:25], v[80:81], v[52:53], v[56:57]
	v_cvt_pk_bf16_f32 v238, v18, v19
	v_cvt_pk_bf16_f32 v239, v20, v21
	v_cvt_pk_bf16_f32 v240, v22, v23
	v_cvt_pk_bf16_f32 v241, v24, v25
	global_store_dwordx2 v[74:75], v[238:239], off offset:1536
	global_store_dwordx2 v[76:77], v[240:241], off offset:1536
	v_pk_mul_f32 v[80:81], v[10:11], v[78:79] op_sel_hi:[1,0]
	v_pk_mul_f32 v[82:83], v[12:13], v[78:79] op_sel_hi:[1,0]
	s_waitcnt vmcnt(8)
	v_pk_fma_f32 v[10:11], v[16:17], v[222:223], v[226:227]
	v_pk_fma_f32 v[12:13], v[14:15], v[224:225], v[228:229]
	v_pk_fma_f32 v[14:15], v[82:83], v[222:223], v[226:227]
	v_pk_fma_f32 v[16:17], v[80:81], v[224:225], v[228:229]
	v_cvt_pk_bf16_f32 v238, v10, v11
	v_cvt_pk_bf16_f32 v239, v12, v13
	v_cvt_pk_bf16_f32 v240, v14, v15
	v_cvt_pk_bf16_f32 v241, v16, v17
	global_store_dwordx2 v[74:75], v[238:239], off offset:2048
	global_store_dwordx2 v[76:77], v[240:241], off offset:2048
	v_pk_mul_f32 v[80:81], v[34:35], v[78:79] op_sel_hi:[1,0]
	v_pk_mul_f32 v[82:83], v[36:37], v[78:79] op_sel_hi:[1,0]
	s_waitcnt vmcnt(6)
	v_pk_fma_f32 v[34:35], v[44:45], v[230:231], v[234:235]
	v_pk_fma_f32 v[36:37], v[42:43], v[232:233], v[236:237]
	v_pk_fma_f32 v[42:43], v[82:83], v[230:231], v[234:235]
	v_pk_fma_f32 v[44:45], v[80:81], v[232:233], v[236:237]
	v_cvt_pk_bf16_f32 v238, v34, v35
	v_cvt_pk_bf16_f32 v239, v36, v37
	v_cvt_pk_bf16_f32 v240, v42, v43
	v_cvt_pk_bf16_f32 v241, v44, v45
	global_store_dwordx2 v[74:75], v[238:239], off offset:2560
	global_store_dwordx2 v[76:77], v[240:241], off offset:2560
	global_load_dwordx4 v[50:53], v[158:159], off
	s_nop 0
	global_load_dwordx4 v[54:57], v[160:161], off
	v_pk_mul_f32 v[80:81], v[62:63], v[78:79] op_sel_hi:[1,0]
	v_pk_mul_f32 v[82:83], v[64:65], v[78:79] op_sel_hi:[1,0]
	s_waitcnt vmcnt(0)
	v_pk_fma_f32 v[62:63], v[68:69], v[50:51], v[54:55]
	v_pk_fma_f32 v[64:65], v[66:67], v[52:53], v[56:57]
	v_pk_fma_f32 v[50:51], v[82:83], v[50:51], v[54:55]
	v_pk_fma_f32 v[52:53], v[80:81], v[52:53], v[56:57]
	v_cvt_pk_bf16_f32 v54, v62, v63
	v_cvt_pk_bf16_f32 v55, v64, v65
	v_cvt_pk_bf16_f32 v56, v50, v51
	v_cvt_pk_bf16_f32 v57, v52, v53
	global_store_dwordx2 v[74:75], v[54:55], off offset:3072
	global_store_dwordx2 v[76:77], v[56:57], off offset:3072
	global_load_dwordx4 v[54:57], v[162:163], off
	s_nop 0
	global_load_dwordx4 v[66:69], v[164:165], off
	ds_write_b128 v111, v[2:5]
	ds_write_b128 v111, v[6:9] offset:8208
	ds_write_b128 v111, v[38:41] offset:1024
	ds_write_b128 v111, v[46:49] offset:9232
	ds_write_b128 v111, v[26:29] offset:2048
	ds_write_b128 v111, v[30:33] offset:10256
	ds_write_b128 v111, v[18:21] offset:3072
	ds_write_b128 v111, v[22:25] offset:11280
	ds_write_b128 v111, v[10:13] offset:4096
	ds_write_b128 v111, v[14:17] offset:12304
	ds_write_b128 v111, v[34:37] offset:5120
	ds_write_b128 v111, v[42:45] offset:13328
	ds_write_b128 v111, v[62:65] offset:6144
	ds_write_b128 v111, v[50:53] offset:14352
	s_waitcnt vmcnt(0)
	v_pk_fma_f32 v[2:3], v[72:73], v[54:55], v[66:67]
	v_pk_fma_f32 v[4:5], v[70:71], v[56:57], v[68:69]
	v_pk_fma_f32 v[6:7], v[60:61], v[54:55], v[66:67]
	v_pk_fma_f32 v[8:9], v[58:59], v[56:57], v[68:69]
	v_cvt_pk_bf16_f32 v10, v2, v3
	v_cvt_pk_bf16_f32 v11, v4, v5
	v_cvt_pk_bf16_f32 v12, v6, v7
	v_cvt_pk_bf16_f32 v13, v8, v9
	ds_write_b128 v111, v[2:5] offset:7168
	ds_write_b128 v111, v[6:9] offset:15376
	global_store_dwordx2 v[74:75], v[10:11], off offset:3584
	global_store_dwordx2 v[76:77], v[12:13], off offset:3584
	s_waitcnt lgkmcnt(0)
	s_barrier
; #define LAS __attribute__((address_space(3)))
; #define LG_LOAD(set_, blk_) do { _Pragma("unroll") for (int f_ = 0; f_ < 10; ++f_) set_[f_] = __builtin_amdgcn_raw_buffer_load_b128(rW, lane * 16, ((wu * 8 + (blk_)) * 10 + f_) * 1024, 0); } while (0)
; __device__ __forceinline__ void phase7(const Args& a, LAS unsigned char* lds, int tid, int lane, int wave) {
;     ...
;             const LAS float* ap = H2 + i * HP + 256 * wave + 8 * g;
;             const int wu = __builtin_amdgcn_readfirstlane(wave);
;             v4u bq0[10], bq1[10];
;     ...
;             LG_LOAD(bq0, 0);
; #pragma unroll
;             for (int b2 = 0; b2 < 4; ++b2) {
;                 LG_LOAD(bq1, 2 * b2 + 1); LG_STEP(bq0, 2 * b2); __builtin_amdgcn_sched_barrier(0);
;                 if (b2 < 3) LG_LOAD(bq0, 2 * b2 + 2);
;                 LG_STEP(bq1, 2 * b2 + 1); __builtin_amdgcn_sched_barrier(0);
	buffer_load_dwordx4 v[2:5], v110, s[24:27], s61 offen
	buffer_load_dwordx4 v[6:9], v110, s[24:27], s0 offen
	s_or_b32 s0, s61, 0x1000
	buffer_load_dwordx4 v[10:13], v110, s[24:27], s0 offen
	s_or_b32 s0, s61, 0x1800
	buffer_load_dwordx4 v[14:17], v110, s[24:27], s0 offen
	ds_read_b128 v[18:21], v188
	ds_read_b128 v[22:25], v188 offset:16
	s_or_b32 s0, s61, 0x2000
	buffer_load_dwordx4 v[26:29], v110, s[24:27], s0 offen
	s_waitcnt lgkmcnt(1)
	v_cvt_pk_bf16_f32 v30, v18, v19
	v_cvt_pk_bf16_f32 v31, v20, v21
	s_waitcnt lgkmcnt(0)
	v_cvt_pk_bf16_f32 v32, v22, v23
	v_cvt_pk_bf16_f32 v33, v24, v25
	v_lshlrev_b32_e32 v34, 16, v30
	v_and_b32_e32 v35, 0xffff0000, v30
	v_lshlrev_b32_e32 v36, 16, v31
	v_and_b32_e32 v37, 0xffff0000, v31
	v_lshlrev_b32_e32 v38, 16, v32
	v_and_b32_e32 v39, 0xffff0000, v32
	v_lshlrev_b32_e32 v40, 16, v33
	v_and_b32_e32 v41, 0xffff0000, v33
	v_pk_add_f32 v[18:19], v[18:19], v[34:35] neg_lo:[0,1] neg_hi:[0,1]
	v_pk_add_f32 v[20:21], v[20:21], v[36:37] neg_lo:[0,1] neg_hi:[0,1]
	v_pk_add_f32 v[22:23], v[22:23], v[38:39] neg_lo:[0,1] neg_hi:[0,1]
	v_pk_add_f32 v[24:25], v[24:25], v[40:41] neg_lo:[0,1] neg_hi:[0,1]
	v_cvt_pk_bf16_f32 v18, v18, v19
	v_cvt_pk_bf16_f32 v19, v20, v21
	v_cvt_pk_bf16_f32 v20, v22, v23
	v_cvt_pk_bf16_f32 v21, v24, v25
	buffer_load_dwordx4 v[22:25], v110, s[24:27], s62 offen
	s_or_b32 s0, s61, 0xc00
	buffer_load_dwordx4 v[38:41], v110, s[24:27], s0 offen
	s_or_b32 s0, s61, 0x1400
	buffer_load_dwordx4 v[46:49], v110, s[24:27], s0 offen
	s_or_b32 s0, s61, 0x1c00
	buffer_load_dwordx4 v[54:57], v110, s[24:27], s0 offen
	s_or_b32 s0, s61, 0x2400
	buffer_load_dwordx4 v[62:65], v110, s[24:27], s0 offen
	s_waitcnt vmcnt(9)
	v_mfma_f32_16x16x32_bf16 v[34:37], v[18:21], v[2:5], 0
	s_or_b32 s0, s61, 0x2800
	s_waitcnt vmcnt(8)
	v_mfma_f32_16x16x32_bf16 v[42:45], v[18:21], v[6:9], 0
	s_waitcnt vmcnt(7)
	v_mfma_f32_16x16x32_bf16 v[50:53], v[18:21], v[10:13], 0
	s_waitcnt vmcnt(6)
	v_mfma_f32_16x16x32_bf16 v[58:61], v[18:21], v[14:17], 0
	s_waitcnt vmcnt(5)
	v_mfma_f32_16x16x32_bf16 v[18:21], v[18:21], v[26:29], 0
	s_waitcnt vmcnt(4)
	v_mfma_f32_16x16x32_bf16 v[22:25], v[30:33], v[22:25], v[34:37]
	s_waitcnt vmcnt(3)
	v_mfma_f32_16x16x32_bf16 v[34:37], v[30:33], v[38:41], v[42:45]
	s_waitcnt vmcnt(2)
	v_mfma_f32_16x16x32_bf16 v[38:41], v[30:33], v[46:49], v[50:53]
	s_waitcnt vmcnt(1)
	v_mfma_f32_16x16x32_bf16 v[42:45], v[30:33], v[54:57], v[58:61]
	s_waitcnt vmcnt(0)
	v_mfma_f32_16x16x32_bf16 v[18:21], v[30:33], v[62:65], v[18:21]
	v_mfma_f32_16x16x32_bf16 v[2:5], v[30:33], v[2:5], v[22:25]
	v_mfma_f32_16x16x32_bf16 v[6:9], v[30:33], v[6:9], v[34:37]
	s_nop 1
	buffer_load_dwordx4 v[22:25], v110, s[24:27], s0 offen
	buffer_load_dwordx4 v[34:37], v110, s[24:27], s1 offen
	buffer_load_dwordx4 v[46:49], v110, s[24:27], s8 offen
	buffer_load_dwordx4 v[50:53], v110, s[24:27], s9 offen
	v_mfma_f32_16x16x32_bf16 v[10:13], v[30:33], v[10:13], v[38:41]
	s_nop 2
	buffer_load_dwordx4 v[38:41], v110, s[24:27], s10 offen
	buffer_load_dwordx4 v[54:57], v110, s[24:27], s11 offen
	buffer_load_dwordx4 v[58:61], v110, s[24:27], s12 offen
	buffer_load_dwordx4 v[62:65], v110, s[24:27], s13 offen
	v_mfma_f32_16x16x32_bf16 v[14:17], v[30:33], v[14:17], v[42:45]
	s_nop 2
	buffer_load_dwordx4 v[42:45], v110, s[24:27], s14 offen
	buffer_load_dwordx4 v[66:69], v110, s[24:27], s15 offen
	v_mfma_f32_16x16x32_bf16 v[18:21], v[30:33], v[26:29], v[18:21]
	ds_read_b128 v[26:29], v188 offset:128
	ds_read_b128 v[30:33], v188 offset:144
	s_add_i32 s8, s61, 0x7000
	s_add_i32 s9, s61, 0x6c00
	s_add_i32 s1, s61, 0x7400
	s_waitcnt lgkmcnt(1)
	v_cvt_pk_bf16_f32 v70, v26, v27
	v_cvt_pk_bf16_f32 v71, v28, v29
	v_lshlrev_b32_e32 v72, 16, v70
	v_and_b32_e32 v73, 0xffff0000, v70
	v_lshlrev_b32_e32 v74, 16, v71
	v_and_b32_e32 v75, 0xffff0000, v71
	v_pk_add_f32 v[26:27], v[26:27], v[72:73] neg_lo:[0,1] neg_hi:[0,1]
	v_pk_add_f32 v[28:29], v[28:29], v[74:75] neg_lo:[0,1] neg_hi:[0,1]
	s_waitcnt lgkmcnt(0)
	v_cvt_pk_bf16_f32 v72, v30, v31
	v_cvt_pk_bf16_f32 v26, v26, v27
	v_cvt_pk_bf16_f32 v27, v28, v29
	v_lshlrev_b32_e32 v28, 16, v72
	v_and_b32_e32 v29, 0xffff0000, v72
	v_cvt_pk_bf16_f32 v73, v32, v33
	v_pk_add_f32 v[28:29], v[30:31], v[28:29] neg_lo:[0,1] neg_hi:[0,1]
	v_lshlrev_b32_e32 v30, 16, v73
	v_and_b32_e32 v31, 0xffff0000, v73
	v_pk_add_f32 v[30:31], v[32:33], v[30:31] neg_lo:[0,1] neg_hi:[0,1]
	v_cvt_pk_bf16_f32 v28, v28, v29
	v_cvt_pk_bf16_f32 v29, v30, v31
	s_add_i32 s0, s61, 0x5000
	s_waitcnt vmcnt(9)
	v_mfma_f32_16x16x32_bf16 v[2:5], v[26:29], v[22:25], v[2:5]
	s_waitcnt vmcnt(5)
	v_mfma_f32_16x16x32_bf16 v[10:13], v[26:29], v[38:41], v[10:13]
	v_mfma_f32_16x16x32_bf16 v[6:9], v[26:29], v[46:49], v[6:9]
	s_waitcnt vmcnt(3)
	v_mfma_f32_16x16x32_bf16 v[14:17], v[26:29], v[58:61], v[14:17]
	v_mfma_f32_16x16x32_bf16 v[2:5], v[70:73], v[34:37], v[2:5]
	v_mfma_f32_16x16x32_bf16 v[10:13], v[70:73], v[54:57], v[10:13]
	v_mfma_f32_16x16x32_bf16 v[6:9], v[70:73], v[50:53], v[6:9]
	s_waitcnt vmcnt(2)
	v_mfma_f32_16x16x32_bf16 v[14:17], v[70:73], v[62:65], v[14:17]
	v_mfma_f32_16x16x32_bf16 v[2:5], v[70:73], v[22:25], v[2:5]
	buffer_load_dwordx4 v[22:25], v110, s[24:27], s8 offen
	buffer_load_dwordx4 v[30:33], v110, s[24:27], s9 offen
	s_add_i32 s8, s61, 0x6800
	s_add_i32 s9, s61, 0x6400
	v_mfma_f32_16x16x32_bf16 v[10:13], v[70:73], v[38:41], v[10:13]
	buffer_load_dwordx4 v[34:37], v110, s[24:27], s8 offen
	buffer_load_dwordx4 v[38:41], v110, s[24:27], s9 offen
	s_add_i32 s8, s61, 0x6000
	s_add_i32 s9, s61, 0x5c00
	v_mfma_f32_16x16x32_bf16 v[6:9], v[70:73], v[46:49], v[6:9]
	buffer_load_dwordx4 v[46:49], v110, s[24:27], s8 offen
	buffer_load_dwordx4 v[50:53], v110, s[24:27], s9 offen
	s_add_i32 s8, s61, 0x5800
	s_add_i32 s9, s61, 0x5400
	v_mfma_f32_16x16x32_bf16 v[14:17], v[70:73], v[58:61], v[14:17]
	s_waitcnt vmcnt(7)
; #define LG_LOAD(set_, blk_) do { _Pragma("unroll") for (int f_ = 0; f_ < 10; ++f_) set_[f_] = __builtin_amdgcn_raw_buffer_load_b128(rW, lane * 16, ((wu * 8 + (blk_)) * 10 + f_) * 1024, 0); } while (0)
; __device__ __forceinline__ void phase7(const Args& a, LAS unsigned char* lds, int tid, int lane, int wave) {
;     ...
;             LG_LOAD(bq0, 0);
; #pragma unroll
;             for (int b2 = 0; b2 < 4; ++b2) {
;                 LG_LOAD(bq1, 2 * b2 + 1); LG_STEP(bq0, 2 * b2); __builtin_amdgcn_sched_barrier(0);
;                 if (b2 < 3) LG_LOAD(bq0, 2 * b2 + 2);
;                 LG_STEP(bq1, 2 * b2 + 1); __builtin_amdgcn_sched_barrier(0);
	v_mfma_f32_16x16x32_bf16 v[18:21], v[26:29], v[42:45], v[18:21]
	buffer_load_dwordx4 v[26:29], v110, s[24:27], s8 offen
	buffer_load_dwordx4 v[54:57], v110, s[24:27], s9 offen
	buffer_load_dwordx4 v[58:61], v110, s[24:27], s1 offen
	buffer_load_dwordx4 v[62:65], v110, s[24:27], s0 offen
	s_waitcnt vmcnt(10)
	v_mfma_f32_16x16x32_bf16 v[18:21], v[70:73], v[66:69], v[18:21]
	v_mfma_f32_16x16x32_bf16 v[18:21], v[70:73], v[42:45], v[18:21]
	ds_read_b128 v[42:45], v188 offset:256
	ds_read_b128 v[66:69], v188 offset:272
	s_add_i32 s0, s61, 0x7800
	s_add_i32 s1, s61, 0x7c00
	s_waitcnt lgkmcnt(1)
	v_cvt_pk_bf16_f32 v70, v42, v43
	v_cvt_pk_bf16_f32 v71, v44, v45
	v_lshlrev_b32_e32 v72, 16, v70
	v_and_b32_e32 v73, 0xffff0000, v70
	v_lshlrev_b32_e32 v74, 16, v71
	v_and_b32_e32 v75, 0xffff0000, v71
	v_pk_add_f32 v[42:43], v[42:43], v[72:73] neg_lo:[0,1] neg_hi:[0,1]
	v_pk_add_f32 v[44:45], v[44:45], v[74:75] neg_lo:[0,1] neg_hi:[0,1]
	s_waitcnt lgkmcnt(0)
	v_cvt_pk_bf16_f32 v72, v66, v67
	v_cvt_pk_bf16_f32 v42, v42, v43
	v_cvt_pk_bf16_f32 v43, v44, v45
	v_lshlrev_b32_e32 v44, 16, v72
	v_and_b32_e32 v45, 0xffff0000, v72
	v_cvt_pk_bf16_f32 v73, v68, v69
	v_pk_add_f32 v[44:45], v[66:67], v[44:45] neg_lo:[0,1] neg_hi:[0,1]
	v_lshlrev_b32_e32 v66, 16, v73
	v_and_b32_e32 v67, 0xffff0000, v73
	v_pk_add_f32 v[66:67], v[68:69], v[66:67] neg_lo:[0,1] neg_hi:[0,1]
	v_cvt_pk_bf16_f32 v44, v44, v45
	v_cvt_pk_bf16_f32 v45, v66, v67
	s_waitcnt vmcnt(3)
	s_nop 0
	v_mfma_f32_16x16x32_bf16 v[6:9], v[42:45], v[26:29], v[6:9]
	v_mfma_f32_16x16x32_bf16 v[10:13], v[42:45], v[46:49], v[10:13]
	v_mfma_f32_16x16x32_bf16 v[14:17], v[42:45], v[34:37], v[14:17]
	s_waitcnt vmcnt(0)
	v_mfma_f32_16x16x32_bf16 v[2:5], v[42:45], v[62:65], v[2:5]
	v_mfma_f32_16x16x32_bf16 v[6:9], v[70:73], v[50:53], v[6:9]
	v_mfma_f32_16x16x32_bf16 v[10:13], v[70:73], v[38:41], v[10:13]
	v_mfma_f32_16x16x32_bf16 v[14:17], v[70:73], v[30:33], v[14:17]
	v_mfma_f32_16x16x32_bf16 v[2:5], v[70:73], v[54:57], v[2:5]
	v_mfma_f32_16x16x32_bf16 v[6:9], v[70:73], v[26:29], v[6:9]
	buffer_load_dwordx4 v[26:29], v110, s[24:27], s0 offen
	buffer_load_dwordx4 v[38:41], v110, s[24:27], s1 offen
	s_add_i32 s0, s61, 0x8000
	s_add_i32 s1, s61, 0x8400
	v_mfma_f32_16x16x32_bf16 v[18:21], v[42:45], v[22:25], v[18:21]
	v_mfma_f32_16x16x32_bf16 v[10:13], v[70:73], v[46:49], v[10:13]
	buffer_load_dwordx4 v[30:33], v110, s[24:27], s0 offen
	buffer_load_dwordx4 v[46:49], v110, s[24:27], s1 offen
	s_add_i32 s0, s61, 0x8800
	s_add_i32 s1, s61, 0x8c00
	v_mfma_f32_16x16x32_bf16 v[14:17], v[70:73], v[34:37], v[14:17]
	buffer_load_dwordx4 v[34:37], v110, s[24:27], s0 offen
	buffer_load_dwordx4 v[50:53], v110, s[24:27], s1 offen
	s_add_i32 s0, s61, 0x9000
	s_add_i32 s1, s61, 0x9400
	buffer_load_dwordx4 v[42:45], v110, s[24:27], s0 offen
	buffer_load_dwordx4 v[54:57], v110, s[24:27], s1 offen
	s_add_i32 s0, s61, 0x9800
	v_mfma_f32_16x16x32_bf16 v[2:5], v[70:73], v[62:65], v[2:5]
	s_add_i32 s1, s61, 0x9c00
	v_mfma_f32_16x16x32_bf16 v[18:21], v[70:73], v[58:61], v[18:21]
	buffer_load_dwordx4 v[58:61], v110, s[24:27], s0 offen
	buffer_load_dwordx4 v[62:65], v110, s[24:27], s1 offen
	v_mfma_f32_16x16x32_bf16 v[18:21], v[70:73], v[22:25], v[18:21]
	ds_read_b128 v[22:25], v188 offset:384
	ds_read_b128 v[66:69], v188 offset:400
	s_add_i32 s0, s61, 0xc400
	s_add_i32 s1, s61, 0xc000
	s_waitcnt lgkmcnt(1)
	v_cvt_pk_bf16_f32 v70, v22, v23
	v_cvt_pk_bf16_f32 v71, v24, v25
	v_lshlrev_b32_e32 v72, 16, v70
	v_and_b32_e32 v73, 0xffff0000, v70
	v_lshlrev_b32_e32 v74, 16, v71
	v_and_b32_e32 v75, 0xffff0000, v71
	v_pk_add_f32 v[22:23], v[22:23], v[72:73] neg_lo:[0,1] neg_hi:[0,1]
	v_pk_add_f32 v[24:25], v[24:25], v[74:75] neg_lo:[0,1] neg_hi:[0,1]
	s_waitcnt lgkmcnt(0)
	v_cvt_pk_bf16_f32 v72, v66, v67
	v_cvt_pk_bf16_f32 v22, v22, v23
	v_cvt_pk_bf16_f32 v23, v24, v25
	v_lshlrev_b32_e32 v24, 16, v72
	v_and_b32_e32 v25, 0xffff0000, v72
	v_cvt_pk_bf16_f32 v73, v68, v69
	v_pk_add_f32 v[24:25], v[66:67], v[24:25] neg_lo:[0,1] neg_hi:[0,1]
	v_lshlrev_b32_e32 v66, 16, v73
	v_and_b32_e32 v67, 0xffff0000, v73
	v_pk_add_f32 v[66:67], v[68:69], v[66:67] neg_lo:[0,1] neg_hi:[0,1]
	v_cvt_pk_bf16_f32 v24, v24, v25
	v_cvt_pk_bf16_f32 v25, v66, v67
	s_waitcnt vmcnt(9)
	s_nop 0
	v_mfma_f32_16x16x32_bf16 v[2:5], v[22:25], v[26:29], v[2:5]
	s_waitcnt vmcnt(7)
	v_mfma_f32_16x16x32_bf16 v[6:9], v[22:25], v[30:33], v[6:9]
	s_waitcnt vmcnt(5)
	v_mfma_f32_16x16x32_bf16 v[10:13], v[22:25], v[34:37], v[10:13]
	s_waitcnt vmcnt(3)
	v_mfma_f32_16x16x32_bf16 v[14:17], v[22:25], v[42:45], v[14:17]
	v_mfma_f32_16x16x32_bf16 v[2:5], v[70:73], v[38:41], v[2:5]
	v_mfma_f32_16x16x32_bf16 v[6:9], v[70:73], v[46:49], v[6:9]
	v_mfma_f32_16x16x32_bf16 v[10:13], v[70:73], v[50:53], v[10:13]
	s_waitcnt vmcnt(2)
	v_mfma_f32_16x16x32_bf16 v[14:17], v[70:73], v[54:57], v[14:17]
	v_mfma_f32_16x16x32_bf16 v[2:5], v[70:73], v[26:29], v[2:5]
	v_mfma_f32_16x16x32_bf16 v[6:9], v[70:73], v[30:33], v[6:9]
	buffer_load_dwordx4 v[26:29], v110, s[24:27], s0 offen
	buffer_load_dwordx4 v[30:33], v110, s[24:27], s1 offen
	s_add_i32 s0, s61, 0xbc00
	s_add_i32 s1, s61, 0xb800
	s_waitcnt vmcnt(3)
	v_mfma_f32_16x16x32_bf16 v[18:21], v[22:25], v[58:61], v[18:21]
	v_mfma_f32_16x16x32_bf16 v[10:13], v[70:73], v[34:37], v[10:13]
	buffer_load_dwordx4 v[34:37], v110, s[24:27], s0 offen
	buffer_load_dwordx4 v[38:41], v110, s[24:27], s1 offen
	s_add_i32 s0, s61, 0xb400
	s_add_i32 s1, s61, 0xb000
	v_mfma_f32_16x16x32_bf16 v[14:17], v[70:73], v[42:45], v[14:17]
	buffer_load_dwordx4 v[42:45], v110, s[24:27], s0 offen
	buffer_load_dwordx4 v[46:49], v110, s[24:27], s1 offen
	s_add_i32 s0, s61, 0xac00
	s_add_i32 s1, s61, 0xa800
	buffer_load_dwordx4 v[22:25], v110, s[24:27], s0 offen
	buffer_load_dwordx4 v[50:53], v110, s[24:27], s1 offen
	s_add_i32 s0, s61, 0xa400
	s_add_i32 s1, s61, 0xa000
	s_waitcnt vmcnt(8)
; #define LG_LOAD(set_, blk_) do { _Pragma("unroll") for (int f_ = 0; f_ < 10; ++f_) set_[f_] = __builtin_amdgcn_raw_buffer_load_b128(rW, lane * 16, ((wu * 8 + (blk_)) * 10 + f_) * 1024, 0); } while (0)
; __device__ __forceinline__ void phase7(const Args& a, LAS unsigned char* lds, int tid, int lane, int wave) {
;     ...
;             LG_LOAD(bq0, 0);
; #pragma unroll
;             for (int b2 = 0; b2 < 4; ++b2) {
;                 LG_LOAD(bq1, 2 * b2 + 1); LG_STEP(bq0, 2 * b2); __builtin_amdgcn_sched_barrier(0);
;                 if (b2 < 3) LG_LOAD(bq0, 2 * b2 + 2);
;                 LG_STEP(bq1, 2 * b2 + 1); __builtin_amdgcn_sched_barrier(0);
	v_mfma_f32_16x16x32_bf16 v[18:21], v[70:73], v[62:65], v[18:21]
	buffer_load_dwordx4 v[54:57], v110, s[24:27], s0 offen
	buffer_load_dwordx4 v[62:65], v110, s[24:27], s1 offen
	v_mfma_f32_16x16x32_bf16 v[18:21], v[70:73], v[58:61], v[18:21]
	ds_read_b128 v[58:61], v188 offset:512
	ds_read_b128 v[66:69], v188 offset:528
	s_add_i32 s0, s61, 0xc800
	s_add_i32 s1, s61, 0xcc00
	s_waitcnt lgkmcnt(1)
	v_cvt_pk_bf16_f32 v70, v58, v59
	v_cvt_pk_bf16_f32 v71, v60, v61
	v_lshlrev_b32_e32 v72, 16, v70
	v_and_b32_e32 v73, 0xffff0000, v70
	v_lshlrev_b32_e32 v74, 16, v71
	v_and_b32_e32 v75, 0xffff0000, v71
	v_pk_add_f32 v[58:59], v[58:59], v[72:73] neg_lo:[0,1] neg_hi:[0,1]
	v_pk_add_f32 v[60:61], v[60:61], v[74:75] neg_lo:[0,1] neg_hi:[0,1]
	s_waitcnt lgkmcnt(0)
	v_cvt_pk_bf16_f32 v72, v66, v67
	v_cvt_pk_bf16_f32 v58, v58, v59
	v_cvt_pk_bf16_f32 v59, v60, v61
	v_lshlrev_b32_e32 v60, 16, v72
	v_and_b32_e32 v61, 0xffff0000, v72
	v_cvt_pk_bf16_f32 v73, v68, v69
	v_pk_add_f32 v[60:61], v[66:67], v[60:61] neg_lo:[0,1] neg_hi:[0,1]
	v_lshlrev_b32_e32 v66, 16, v73
	v_and_b32_e32 v67, 0xffff0000, v73
	v_pk_add_f32 v[66:67], v[68:69], v[66:67] neg_lo:[0,1] neg_hi:[0,1]
	v_cvt_pk_bf16_f32 v60, v60, v61
	v_cvt_pk_bf16_f32 v61, v66, v67
	s_waitcnt vmcnt(4)
	s_nop 0
	v_mfma_f32_16x16x32_bf16 v[10:13], v[58:61], v[46:49], v[10:13]
	s_waitcnt vmcnt(2)
	v_mfma_f32_16x16x32_bf16 v[6:9], v[58:61], v[50:53], v[6:9]
	v_mfma_f32_16x16x32_bf16 v[14:17], v[58:61], v[38:41], v[14:17]
	s_waitcnt vmcnt(0)
	v_mfma_f32_16x16x32_bf16 v[2:5], v[58:61], v[62:65], v[2:5]
	v_mfma_f32_16x16x32_bf16 v[10:13], v[70:73], v[42:45], v[10:13]
	v_mfma_f32_16x16x32_bf16 v[6:9], v[70:73], v[22:25], v[6:9]
	buffer_load_dwordx4 v[22:25], v110, s[24:27], s0 offen
	buffer_load_dwordx4 v[42:45], v110, s[24:27], s1 offen
	s_add_i32 s0, s61, 0xd000
	s_add_i32 s1, s61, 0xd400
	v_mfma_f32_16x16x32_bf16 v[14:17], v[70:73], v[34:37], v[14:17]
	v_mfma_f32_16x16x32_bf16 v[2:5], v[70:73], v[54:57], v[2:5]
	v_mfma_f32_16x16x32_bf16 v[18:21], v[58:61], v[30:33], v[18:21]
	v_mfma_f32_16x16x32_bf16 v[10:13], v[70:73], v[46:49], v[10:13]
	buffer_load_dwordx4 v[34:37], v110, s[24:27], s0 offen
	buffer_load_dwordx4 v[46:49], v110, s[24:27], s1 offen
	s_add_i32 s0, s61, 0xd800
	s_add_i32 s1, s61, 0xdc00
	v_mfma_f32_16x16x32_bf16 v[6:9], v[70:73], v[50:53], v[6:9]
	v_mfma_f32_16x16x32_bf16 v[14:17], v[70:73], v[38:41], v[14:17]
	buffer_load_dwordx4 v[38:41], v110, s[24:27], s0 offen
	buffer_load_dwordx4 v[50:53], v110, s[24:27], s1 offen
	s_add_i32 s0, s61, 0xe000
	s_add_i32 s1, s61, 0xe400
	buffer_load_dwordx4 v[54:57], v110, s[24:27], s0 offen
	buffer_load_dwordx4 v[58:61], v110, s[24:27], s1 offen
	s_add_i32 s0, s61, 0xe800
	v_mfma_f32_16x16x32_bf16 v[2:5], v[70:73], v[62:65], v[2:5]
	s_add_i32 s1, s61, 0xec00
	v_mfma_f32_16x16x32_bf16 v[18:21], v[70:73], v[26:29], v[18:21]
	buffer_load_dwordx4 v[26:29], v110, s[24:27], s0 offen
	buffer_load_dwordx4 v[62:65], v110, s[24:27], s1 offen
	v_mfma_f32_16x16x32_bf16 v[18:21], v[70:73], v[30:33], v[18:21]
	ds_read_b128 v[30:33], v188 offset:640
	ds_read_b128 v[66:69], v188 offset:656
	s_add_i32 s0, s61, 0x11400
	s_add_i32 s1, s61, 0x11000
	s_waitcnt lgkmcnt(1)
	v_cvt_pk_bf16_f32 v70, v30, v31
	v_cvt_pk_bf16_f32 v71, v32, v33
	v_lshlrev_b32_e32 v72, 16, v70
	v_and_b32_e32 v73, 0xffff0000, v70
	v_lshlrev_b32_e32 v74, 16, v71
	v_and_b32_e32 v75, 0xffff0000, v71
	v_pk_add_f32 v[30:31], v[30:31], v[72:73] neg_lo:[0,1] neg_hi:[0,1]
	v_pk_add_f32 v[32:33], v[32:33], v[74:75] neg_lo:[0,1] neg_hi:[0,1]
	s_waitcnt lgkmcnt(0)
	v_cvt_pk_bf16_f32 v72, v66, v67
	v_cvt_pk_bf16_f32 v30, v30, v31
	v_cvt_pk_bf16_f32 v31, v32, v33
	v_lshlrev_b32_e32 v32, 16, v72
	v_and_b32_e32 v33, 0xffff0000, v72
	v_cvt_pk_bf16_f32 v73, v68, v69
	v_pk_add_f32 v[32:33], v[66:67], v[32:33] neg_lo:[0,1] neg_hi:[0,1]
	v_lshlrev_b32_e32 v66, 16, v73
	v_and_b32_e32 v67, 0xffff0000, v73
	v_pk_add_f32 v[66:67], v[68:69], v[66:67] neg_lo:[0,1] neg_hi:[0,1]
	v_cvt_pk_bf16_f32 v32, v32, v33
	v_cvt_pk_bf16_f32 v33, v66, v67
	s_waitcnt vmcnt(9)
	s_nop 0
	v_mfma_f32_16x16x32_bf16 v[2:5], v[30:33], v[22:25], v[2:5]
	s_waitcnt vmcnt(7)
	v_mfma_f32_16x16x32_bf16 v[6:9], v[30:33], v[34:37], v[6:9]
	s_waitcnt vmcnt(5)
	v_mfma_f32_16x16x32_bf16 v[10:13], v[30:33], v[38:41], v[10:13]
	s_waitcnt vmcnt(3)
	v_mfma_f32_16x16x32_bf16 v[14:17], v[30:33], v[54:57], v[14:17]
	v_mfma_f32_16x16x32_bf16 v[2:5], v[70:73], v[42:45], v[2:5]
	v_mfma_f32_16x16x32_bf16 v[6:9], v[70:73], v[46:49], v[6:9]
	v_mfma_f32_16x16x32_bf16 v[10:13], v[70:73], v[50:53], v[10:13]
	s_waitcnt vmcnt(2)
	v_mfma_f32_16x16x32_bf16 v[14:17], v[70:73], v[58:61], v[14:17]
	v_mfma_f32_16x16x32_bf16 v[2:5], v[70:73], v[22:25], v[2:5]
	v_mfma_f32_16x16x32_bf16 v[6:9], v[70:73], v[34:37], v[6:9]
	buffer_load_dwordx4 v[22:25], v110, s[24:27], s0 offen
	buffer_load_dwordx4 v[34:37], v110, s[24:27], s1 offen
	s_add_i32 s0, s61, 0x10c00
	s_add_i32 s1, s61, 0x10800
	s_waitcnt vmcnt(3)
	v_mfma_f32_16x16x32_bf16 v[18:21], v[30:33], v[26:29], v[18:21]
	v_mfma_f32_16x16x32_bf16 v[10:13], v[70:73], v[38:41], v[10:13]
	buffer_load_dwordx4 v[38:41], v110, s[24:27], s0 offen
	buffer_load_dwordx4 v[42:45], v110, s[24:27], s1 offen
	s_add_i32 s0, s61, 0x10400
	s_add_i32 s1, s61, 0x10000
	buffer_load_dwordx4 v[46:49], v110, s[24:27], s0 offen
	buffer_load_dwordx4 v[50:53], v110, s[24:27], s1 offen
	s_add_i32 s0, s61, 0xfc00
	v_mfma_f32_16x16x32_bf16 v[14:17], v[70:73], v[54:57], v[14:17]
	s_add_i32 s1, s61, 0xf800
	buffer_load_dwordx4 v[30:33], v110, s[24:27], s0 offen
	buffer_load_dwordx4 v[54:57], v110, s[24:27], s1 offen
	s_add_i32 s0, s61, 0xf400
	s_add_i32 s1, s61, 0xf000
	s_waitcnt vmcnt(8)
; #define LAS __attribute__((address_space(3)))
; #define LG_LOAD(set_, blk_) do { _Pragma("unroll") for (int f_ = 0; f_ < 10; ++f_) set_[f_] = __builtin_amdgcn_raw_buffer_load_b128(rW, lane * 16, ((wu * 8 + (blk_)) * 10 + f_) * 1024, 0); } while (0)
; __device__ __forceinline__ void phase7(const Args& a, LAS unsigned char* lds, int tid, int lane, int wave) {
;     ...
;             LG_LOAD(bq0, 0);
; #pragma unroll
;             for (int b2 = 0; b2 < 4; ++b2) {
;                 LG_LOAD(bq1, 2 * b2 + 1); LG_STEP(bq0, 2 * b2); __builtin_amdgcn_sched_barrier(0);
;                 if (b2 < 3) LG_LOAD(bq0, 2 * b2 + 2);
;                 LG_STEP(bq1, 2 * b2 + 1); __builtin_amdgcn_sched_barrier(0);
;             }
;     ...
;             __syncthreads();
;             LAS float* PART = H2 + wave * (16 * 80);
; #pragma unroll
;             for (int nt = 0; nt < 5; ++nt)
; #pragma unroll
;                 for (int r = 0; r < 4; ++r) PART[(4 * g + r) * 80 + 16 * nt + i] = lacc[nt][r];
;             __syncthreads();
	v_mfma_f32_16x16x32_bf16 v[18:21], v[70:73], v[62:65], v[18:21]
	buffer_load_dwordx4 v[58:61], v110, s[24:27], s0 offen
	buffer_load_dwordx4 v[62:65], v110, s[24:27], s1 offen
	v_mfma_f32_16x16x32_bf16 v[18:21], v[70:73], v[26:29], v[18:21]
	ds_read_b128 v[26:29], v188 offset:768
	ds_read_b128 v[66:69], v188 offset:784
	s_add_i32 s0, s61, 0x11800
	s_add_i32 s1, s61, 0x11c00
	s_waitcnt lgkmcnt(1)
	v_cvt_pk_bf16_f32 v70, v26, v27
	v_cvt_pk_bf16_f32 v71, v28, v29
	v_lshlrev_b32_e32 v72, 16, v70
	v_and_b32_e32 v73, 0xffff0000, v70
	v_lshlrev_b32_e32 v74, 16, v71
	v_and_b32_e32 v75, 0xffff0000, v71
	v_pk_add_f32 v[26:27], v[26:27], v[72:73] neg_lo:[0,1] neg_hi:[0,1]
	v_pk_add_f32 v[28:29], v[28:29], v[74:75] neg_lo:[0,1] neg_hi:[0,1]
	s_waitcnt lgkmcnt(0)
	v_cvt_pk_bf16_f32 v72, v66, v67
	v_cvt_pk_bf16_f32 v26, v26, v27
	v_cvt_pk_bf16_f32 v27, v28, v29
	v_lshlrev_b32_e32 v28, 16, v72
	v_and_b32_e32 v29, 0xffff0000, v72
	v_cvt_pk_bf16_f32 v73, v68, v69
	v_pk_add_f32 v[28:29], v[66:67], v[28:29] neg_lo:[0,1] neg_hi:[0,1]
	v_lshlrev_b32_e32 v66, 16, v73
	v_and_b32_e32 v67, 0xffff0000, v73
	v_pk_add_f32 v[66:67], v[68:69], v[66:67] neg_lo:[0,1] neg_hi:[0,1]
	v_cvt_pk_bf16_f32 v28, v28, v29
	v_cvt_pk_bf16_f32 v29, v66, v67
	s_waitcnt vmcnt(4)
	s_nop 0
	v_mfma_f32_16x16x32_bf16 v[10:13], v[26:29], v[50:53], v[10:13]
	s_waitcnt vmcnt(2)
	v_mfma_f32_16x16x32_bf16 v[6:9], v[26:29], v[54:57], v[6:9]
	v_mfma_f32_16x16x32_bf16 v[14:17], v[26:29], v[42:45], v[14:17]
	s_waitcnt vmcnt(0)
	v_mfma_f32_16x16x32_bf16 v[2:5], v[26:29], v[62:65], v[2:5]
	v_mfma_f32_16x16x32_bf16 v[10:13], v[70:73], v[46:49], v[10:13]
	v_mfma_f32_16x16x32_bf16 v[6:9], v[70:73], v[30:33], v[6:9]
	buffer_load_dwordx4 v[30:33], v110, s[24:27], s0 offen
	buffer_load_dwordx4 v[46:49], v110, s[24:27], s1 offen
	s_add_i32 s0, s61, 0x12000
	s_add_i32 s1, s61, 0x12400
	v_mfma_f32_16x16x32_bf16 v[14:17], v[70:73], v[38:41], v[14:17]
	v_mfma_f32_16x16x32_bf16 v[2:5], v[70:73], v[58:61], v[2:5]
	v_mfma_f32_16x16x32_bf16 v[18:21], v[26:29], v[34:37], v[18:21]
	v_mfma_f32_16x16x32_bf16 v[10:13], v[70:73], v[50:53], v[10:13]
	buffer_load_dwordx4 v[38:41], v110, s[24:27], s0 offen
	buffer_load_dwordx4 v[50:53], v110, s[24:27], s1 offen
	s_add_i32 s0, s61, 0x12800
	s_add_i32 s1, s61, 0x12c00
	v_mfma_f32_16x16x32_bf16 v[6:9], v[70:73], v[54:57], v[6:9]
	v_mfma_f32_16x16x32_bf16 v[14:17], v[70:73], v[42:45], v[14:17]
	buffer_load_dwordx4 v[42:45], v110, s[24:27], s0 offen
	buffer_load_dwordx4 v[54:57], v110, s[24:27], s1 offen
	s_add_i32 s0, s61, 0x13000
	s_add_i32 s1, s61, 0x13400
	buffer_load_dwordx4 v[26:29], v110, s[24:27], s0 offen
	buffer_load_dwordx4 v[58:61], v110, s[24:27], s1 offen
	s_add_i32 s0, s61, 0x13800
	v_mfma_f32_16x16x32_bf16 v[2:5], v[70:73], v[62:65], v[2:5]
	s_add_i32 s1, s61, 0x13c00
	v_mfma_f32_16x16x32_bf16 v[18:21], v[70:73], v[22:25], v[18:21]
	buffer_load_dwordx4 v[22:25], v110, s[24:27], s0 offen
	buffer_load_dwordx4 v[62:65], v110, s[24:27], s1 offen
	v_mfma_f32_16x16x32_bf16 v[18:21], v[70:73], v[34:37], v[18:21]
	ds_read_b128 v[34:37], v188 offset:896
	ds_read_b128 v[66:69], v188 offset:912
	s_waitcnt lgkmcnt(1)
	v_cvt_pk_bf16_f32 v70, v34, v35
	v_cvt_pk_bf16_f32 v71, v36, v37
	v_lshlrev_b32_e32 v72, 16, v70
	v_and_b32_e32 v73, 0xffff0000, v70
	v_lshlrev_b32_e32 v74, 16, v71
	v_and_b32_e32 v75, 0xffff0000, v71
	v_pk_add_f32 v[34:35], v[34:35], v[72:73] neg_lo:[0,1] neg_hi:[0,1]
	v_pk_add_f32 v[36:37], v[36:37], v[74:75] neg_lo:[0,1] neg_hi:[0,1]
	s_waitcnt lgkmcnt(0)
	v_cvt_pk_bf16_f32 v72, v66, v67
	v_cvt_pk_bf16_f32 v34, v34, v35
	v_cvt_pk_bf16_f32 v35, v36, v37
	v_lshlrev_b32_e32 v36, 16, v72
	v_and_b32_e32 v37, 0xffff0000, v72
	v_cvt_pk_bf16_f32 v73, v68, v69
	v_pk_add_f32 v[36:37], v[66:67], v[36:37] neg_lo:[0,1] neg_hi:[0,1]
	v_lshlrev_b32_e32 v66, 16, v73
	v_and_b32_e32 v67, 0xffff0000, v73
	v_pk_add_f32 v[66:67], v[68:69], v[66:67] neg_lo:[0,1] neg_hi:[0,1]
	v_cvt_pk_bf16_f32 v36, v36, v37
	v_cvt_pk_bf16_f32 v37, v66, v67
	s_waitcnt vmcnt(9)
	s_nop 0
	v_mfma_f32_16x16x32_bf16 v[2:5], v[34:37], v[30:33], v[2:5]
	s_waitcnt vmcnt(7)
	v_mfma_f32_16x16x32_bf16 v[6:9], v[34:37], v[38:41], v[6:9]
	s_waitcnt vmcnt(1)
	v_mfma_f32_16x16x32_bf16 v[18:21], v[34:37], v[22:25], v[18:21]
	v_mfma_f32_16x16x32_bf16 v[2:5], v[70:73], v[46:49], v[2:5]
	v_mfma_f32_16x16x32_bf16 v[6:9], v[70:73], v[50:53], v[6:9]
	v_mfma_f32_16x16x32_bf16 v[10:13], v[34:37], v[42:45], v[10:13]
	v_mfma_f32_16x16x32_bf16 v[14:17], v[34:37], v[26:29], v[14:17]
	s_waitcnt vmcnt(0)
	v_mfma_f32_16x16x32_bf16 v[18:21], v[70:73], v[62:65], v[18:21]
	v_mfma_f32_16x16x32_bf16 v[2:5], v[70:73], v[30:33], v[2:5]
	v_mfma_f32_16x16x32_bf16 v[6:9], v[70:73], v[38:41], v[6:9]
	v_mfma_f32_16x16x32_bf16 v[10:13], v[70:73], v[54:57], v[10:13]
	v_mfma_f32_16x16x32_bf16 v[14:17], v[70:73], v[58:61], v[14:17]
	v_mfma_f32_16x16x32_bf16 v[18:21], v[70:73], v[22:25], v[18:21]
	v_mfma_f32_16x16x32_bf16 v[10:13], v[70:73], v[42:45], v[10:13]
	v_mfma_f32_16x16x32_bf16 v[14:17], v[70:73], v[26:29], v[14:17]
	s_barrier
	s_nop 1
	ds_write2_b32 v189, v2, v6 offset1:16
	ds_write2_b32 v189, v4, v8 offset0:160 offset1:176
	s_nop 1
	ds_write2_b32 v189, v7, v11 offset0:96 offset1:112
	v_add_u32_e32 v2, 0x400, v189
	ds_write2_b32 v2, v9, v13 offset1:16
	ds_write2_b32 v189, v10, v14 offset0:32 offset1:48
	ds_write2_b32 v189, v12, v16 offset0:192 offset1:208
	ds_write2_b32 v189, v18, v3 offset0:64 offset1:80
	ds_write2_b32 v189, v15, v19 offset0:128 offset1:144
	ds_write2_b32 v189, v20, v5 offset0:224 offset1:240
	ds_write2_b32 v2, v17, v21 offset0:32 offset1:48
	s_mov_b64 s[0:1], 0
	v_mov_b64_e32 v[2:3], v[172:173]
	v_mov_b64_e32 v[4:5], v[0:1]
	v_mov_b64_e32 v[6:7], v[170:171]
	v_mov_b32_e32 v18, v185
	v_mov_b32_e32 v19, v184
	s_waitcnt lgkmcnt(0)
	s_barrier
	s_branch .LBB0_1024

; #define LAS __attribute__((address_space(3)))
; __device__ __forceinline__ unsigned pk2(float lo, float hi) { f32x2_t v = {lo, hi}; bf16x2_t b = __builtin_convertvector(v, bf16x2_t); return __builtin_bit_cast(unsigned, b); }
; __device__ __forceinline__ float swap1(float x) { return __int_as_float(__builtin_amdgcn_update_dpp(0, __float_as_int(x), 0xB1, 0xF, 0xF, true)); }
; template <bool UP>
; __device__ __forceinline__ void xgemm_unit(const Args& a, LAS unsigned char* lds, int e, int s, int cnt, int off_e, int rp, int tid, int lane, int wave) {
;     ...
;                     for (int h = 0; h < 2; ++h) {
; #pragma unroll
;                         for (int m2 = 0; m2 < 2; ++m2)
; #pragma unroll
;                             for (int r = 0; r < 4; ++r) { const int mi = 2 * h + m2, lrow = 16 * m2 + 4 * g + r; const float w = __int_as_float(rinfo[2 * (16 * mi + 4 * g + r) + 1]);
; #pragma unroll
;                                 for (int q = 0; q < 4; ++q) { const float a0 = acc[mi][2 * q][r] * w, a1 = acc[mi][2 * q + 1][r] * w;
;                                     const float got = swap1(odd ? a0 : a1);
;                                     const unsigned pk = odd ? pk2(got, a1) : pk2(a0, got);
;                                     const int col = odd ? (16 * (2 * q + 1) + i - 1) : (16 * (2 * q) + i);
;                                     *(LAS unsigned*)(stg + lrow * 272 + col * 2) = pk; } }
; #pragma unroll 2
;                         for (int jj = 0; jj < 8; ++jj) { const int lrow = (lane >> 4) + 4 * jj, c = lane & 15, row = 64 * cw + 32 * h + lrow;
;                             const v4u o = *(const LAS v4u*)(stg + lrow * 272 + 16 * c);
;                             if (row < nrows) { const int as = rinfo[2 * (32 * h + lrow)]; *(v4u*)(YA + (size_t)as * D + 128 * s + 8 * c) = o; } }
.LBB0_1269:
	v_add_u32_e32 v230, 0x1d000, v79
	ds_read_b32 v220, v230
	ds_read_b32 v221, v230 offset:32
	ds_read_b32 v222, v230 offset:64
	ds_read_b32 v223, v230 offset:96
	ds_read_b32 v224, v230 offset:128
	ds_read_b32 v225, v230 offset:160
	ds_read_b32 v226, v230 offset:192
	ds_read_b32 v227, v230 offset:224
	ds_read_b128 v[188:191], v71
	ds_read_b128 v[192:195], v71 offset:1088
	ds_read_b128 v[196:199], v71 offset:2176
	ds_read_b128 v[200:203], v71 offset:3264
	ds_read_b128 v[204:207], v71 offset:4352
	ds_read_b128 v[208:211], v71 offset:5440
	ds_read_b128 v[212:215], v71 offset:6528
	ds_read_b128 v[216:219], v71 offset:7616
	s_waitcnt lgkmcnt(7)
	v_mov_b32_e32 v231, v162
	v_ashrrev_i32_e32 v229, 31, v220
	v_mov_b32_e32 v228, v220
	v_lshlrev_b64 v[228:229], 12, v[228:229]
	v_cmp_gt_i32_e32 vcc, s86, v231
	v_lshl_add_u64 v[228:229], v[64:65], 0, v[228:229]
	s_and_saveexec_b64 s[0:1], vcc
	global_store_dwordx4 v[228:229], v[188:191], off
	s_or_b64 exec, exec, s[0:1]
	s_waitcnt lgkmcnt(6)
	v_add_u32_e32 v231, 4, v162
	v_ashrrev_i32_e32 v229, 31, v221
	v_mov_b32_e32 v228, v221
	v_lshlrev_b64 v[228:229], 12, v[228:229]
	v_cmp_gt_i32_e32 vcc, s86, v231
	v_lshl_add_u64 v[228:229], v[64:65], 0, v[228:229]
	s_and_saveexec_b64 s[0:1], vcc
	global_store_dwordx4 v[228:229], v[192:195], off
	s_or_b64 exec, exec, s[0:1]
	s_waitcnt lgkmcnt(5)
	v_add_u32_e32 v231, 8, v162
	v_ashrrev_i32_e32 v229, 31, v222
	v_mov_b32_e32 v228, v222
	v_lshlrev_b64 v[228:229], 12, v[228:229]
	v_cmp_gt_i32_e32 vcc, s86, v231
	v_lshl_add_u64 v[228:229], v[64:65], 0, v[228:229]
	s_and_saveexec_b64 s[0:1], vcc
	global_store_dwordx4 v[228:229], v[196:199], off
	s_or_b64 exec, exec, s[0:1]
	s_waitcnt lgkmcnt(4)
	v_add_u32_e32 v231, 12, v162
	v_ashrrev_i32_e32 v229, 31, v223
	v_mov_b32_e32 v228, v223
	v_lshlrev_b64 v[228:229], 12, v[228:229]
	v_cmp_gt_i32_e32 vcc, s86, v231
	v_lshl_add_u64 v[228:229], v[64:65], 0, v[228:229]
	s_and_saveexec_b64 s[0:1], vcc
	global_store_dwordx4 v[228:229], v[200:203], off
	s_or_b64 exec, exec, s[0:1]
	s_waitcnt lgkmcnt(3)
	v_add_u32_e32 v231, 16, v162
	v_ashrrev_i32_e32 v229, 31, v224
	v_mov_b32_e32 v228, v224
	v_lshlrev_b64 v[228:229], 12, v[228:229]
	v_cmp_gt_i32_e32 vcc, s86, v231
	v_lshl_add_u64 v[228:229], v[64:65], 0, v[228:229]
	s_and_saveexec_b64 s[0:1], vcc
	global_store_dwordx4 v[228:229], v[204:207], off
	s_or_b64 exec, exec, s[0:1]
	s_waitcnt lgkmcnt(2)
	v_add_u32_e32 v231, 20, v162
	v_ashrrev_i32_e32 v229, 31, v225
	v_mov_b32_e32 v228, v225
	v_lshlrev_b64 v[228:229], 12, v[228:229]
	v_cmp_gt_i32_e32 vcc, s86, v231
	v_lshl_add_u64 v[228:229], v[64:65], 0, v[228:229]
	s_and_saveexec_b64 s[0:1], vcc
	global_store_dwordx4 v[228:229], v[208:211], off
	s_or_b64 exec, exec, s[0:1]
	s_waitcnt lgkmcnt(1)
	v_add_u32_e32 v231, 24, v162
	v_ashrrev_i32_e32 v229, 31, v226
	v_mov_b32_e32 v228, v226
	v_lshlrev_b64 v[228:229], 12, v[228:229]
	v_cmp_gt_i32_e32 vcc, s86, v231
	v_lshl_add_u64 v[228:229], v[64:65], 0, v[228:229]
	s_and_saveexec_b64 s[0:1], vcc
	global_store_dwordx4 v[228:229], v[212:215], off
	s_or_b64 exec, exec, s[0:1]
	s_waitcnt lgkmcnt(0)
	v_add_u32_e32 v231, 28, v162
	v_ashrrev_i32_e32 v229, 31, v227
	v_mov_b32_e32 v228, v227
	v_lshlrev_b64 v[228:229], 12, v[228:229]
	v_cmp_gt_i32_e32 vcc, s86, v231
	v_lshl_add_u64 v[228:229], v[64:65], 0, v[228:229]
	s_and_saveexec_b64 s[0:1], vcc
	global_store_dwordx4 v[228:229], v[216:219], off
	s_or_b64 exec, exec, s[0:1]
	s_branch .LBB0_1274

; #define LAS __attribute__((address_space(3)))
; __device__ __forceinline__ unsigned pk2(float lo, float hi) { f32x2_t v = {lo, hi}; bf16x2_t b = __builtin_convertvector(v, bf16x2_t); return __builtin_bit_cast(unsigned, b); }
; __device__ __forceinline__ float swap1(float x) { return __int_as_float(__builtin_amdgcn_update_dpp(0, __float_as_int(x), 0xB1, 0xF, 0xF, true)); }
; template <bool UP>
; __device__ __forceinline__ void xgemm_unit(const Args& a, LAS unsigned char* lds, int e, int s, int cnt, int off_e, int rp, int tid, int lane, int wave) {
;     ...
;                     for (int h = 0; h < 2; ++h) {
; #pragma unroll
;                         for (int m2 = 0; m2 < 2; ++m2)
; #pragma unroll
;                             for (int r = 0; r < 4; ++r) { const int mi = 2 * h + m2, lrow = 16 * m2 + 4 * g + r; const float w = __int_as_float(rinfo[2 * (16 * mi + 4 * g + r) + 1]);
; #pragma unroll
;                                 for (int q = 0; q < 4; ++q) { const float a0 = acc[mi][2 * q][r] * w, a1 = acc[mi][2 * q + 1][r] * w;
;                                     const float got = swap1(odd ? a0 : a1);
;                                     const unsigned pk = odd ? pk2(got, a1) : pk2(a0, got);
;                                     const int col = odd ? (16 * (2 * q + 1) + i - 1) : (16 * (2 * q) + i);
;                                     *(LAS unsigned*)(stg + lrow * 272 + col * 2) = pk; } }
; #pragma unroll 2
;                         for (int jj = 0; jj < 8; ++jj) { const int lrow = (lane >> 4) + 4 * jj, c = lane & 15, row = 64 * cw + 32 * h + lrow;
;                             const v4u o = *(const LAS v4u*)(stg + lrow * 272 + 16 * c);
;                             if (row < nrows) { const int as = rinfo[2 * (32 * h + lrow)]; *(v4u*)(YA + (size_t)as * D + 128 * s + 8 * c) = o; } }
.LBB0_1276:
	v_add_u32_e32 v230, 0x1d100, v1
	ds_read_b32 v220, v230
	ds_read_b32 v221, v230 offset:32
	ds_read_b32 v222, v230 offset:64
	ds_read_b32 v223, v230 offset:96
	ds_read_b32 v224, v230 offset:128
	ds_read_b32 v225, v230 offset:160
	ds_read_b32 v226, v230 offset:192
	ds_read_b32 v227, v230 offset:224
	ds_read_b128 v[188:191], v0
	ds_read_b128 v[192:195], v0 offset:1088
	ds_read_b128 v[196:199], v0 offset:2176
	ds_read_b128 v[200:203], v0 offset:3264
	ds_read_b128 v[204:207], v0 offset:4352
	ds_read_b128 v[208:211], v0 offset:5440
	ds_read_b128 v[212:215], v0 offset:6528
	ds_read_b128 v[216:219], v0 offset:7616
	s_waitcnt lgkmcnt(7)
	v_add_u32_e32 v231, 32, v162
	v_ashrrev_i32_e32 v229, 31, v220
	v_mov_b32_e32 v228, v220
	v_lshlrev_b64 v[228:229], 12, v[228:229]
	v_cmp_gt_i32_e32 vcc, s86, v231
	v_lshl_add_u64 v[228:229], v[64:65], 0, v[228:229]
	s_and_saveexec_b64 s[0:1], vcc
	global_store_dwordx4 v[228:229], v[188:191], off
	s_or_b64 exec, exec, s[0:1]
	s_waitcnt lgkmcnt(6)
	v_add_u32_e32 v231, 36, v162
	v_ashrrev_i32_e32 v229, 31, v221
	v_mov_b32_e32 v228, v221
	v_lshlrev_b64 v[228:229], 12, v[228:229]
	v_cmp_gt_i32_e32 vcc, s86, v231
	v_lshl_add_u64 v[228:229], v[64:65], 0, v[228:229]
	s_and_saveexec_b64 s[0:1], vcc
	global_store_dwordx4 v[228:229], v[192:195], off
	s_or_b64 exec, exec, s[0:1]
	s_waitcnt lgkmcnt(5)
	v_add_u32_e32 v231, 40, v162
	v_ashrrev_i32_e32 v229, 31, v222
	v_mov_b32_e32 v228, v222
	v_lshlrev_b64 v[228:229], 12, v[228:229]
	v_cmp_gt_i32_e32 vcc, s86, v231
	v_lshl_add_u64 v[228:229], v[64:65], 0, v[228:229]
	s_and_saveexec_b64 s[0:1], vcc
	global_store_dwordx4 v[228:229], v[196:199], off
	s_or_b64 exec, exec, s[0:1]
	s_waitcnt lgkmcnt(4)
	v_add_u32_e32 v231, 44, v162
	v_ashrrev_i32_e32 v229, 31, v223
	v_mov_b32_e32 v228, v223
	v_lshlrev_b64 v[228:229], 12, v[228:229]
	v_cmp_gt_i32_e32 vcc, s86, v231
	v_lshl_add_u64 v[228:229], v[64:65], 0, v[228:229]
	s_and_saveexec_b64 s[0:1], vcc
	global_store_dwordx4 v[228:229], v[200:203], off
	s_or_b64 exec, exec, s[0:1]
	s_waitcnt lgkmcnt(3)
	v_add_u32_e32 v231, 48, v162
	v_ashrrev_i32_e32 v229, 31, v224
	v_mov_b32_e32 v228, v224
	v_lshlrev_b64 v[228:229], 12, v[228:229]
	v_cmp_gt_i32_e32 vcc, s86, v231
	v_lshl_add_u64 v[228:229], v[64:65], 0, v[228:229]
	s_and_saveexec_b64 s[0:1], vcc
	global_store_dwordx4 v[228:229], v[204:207], off
	s_or_b64 exec, exec, s[0:1]
	s_waitcnt lgkmcnt(2)
	v_add_u32_e32 v231, 52, v162
	v_ashrrev_i32_e32 v229, 31, v225
	v_mov_b32_e32 v228, v225
	v_lshlrev_b64 v[228:229], 12, v[228:229]
	v_cmp_gt_i32_e32 vcc, s86, v231
	v_lshl_add_u64 v[228:229], v[64:65], 0, v[228:229]
	s_and_saveexec_b64 s[0:1], vcc
	global_store_dwordx4 v[228:229], v[208:211], off
	s_or_b64 exec, exec, s[0:1]
	s_waitcnt lgkmcnt(1)
	v_add_u32_e32 v231, 56, v162
	v_ashrrev_i32_e32 v229, 31, v226
	v_mov_b32_e32 v228, v226
	v_lshlrev_b64 v[228:229], 12, v[228:229]
	v_cmp_gt_i32_e32 vcc, s86, v231
	v_lshl_add_u64 v[228:229], v[64:65], 0, v[228:229]
	s_and_saveexec_b64 s[0:1], vcc
	global_store_dwordx4 v[228:229], v[212:215], off
	s_or_b64 exec, exec, s[0:1]
	s_waitcnt lgkmcnt(0)
	v_add_u32_e32 v231, 60, v162
	v_ashrrev_i32_e32 v229, 31, v227
	v_mov_b32_e32 v228, v227
	v_lshlrev_b64 v[228:229], 12, v[228:229]
	v_cmp_gt_i32_e32 vcc, s86, v231
	v_lshl_add_u64 v[228:229], v[64:65], 0, v[228:229]
	s_and_saveexec_b64 s[0:1], vcc
	global_store_dwordx4 v[228:229], v[216:219], off
	s_or_b64 exec, exec, s[0:1]
